# speedup vs baseline: 1.0639x; 1.0306x over previous
attn_fwd_pwg4x64:
	s_load_dwordx2 s[22:23], s[0:1], 0x0
	s_load_dwordx8 s[4:11], s[0:1], 0x8
	s_load_dwordx2 s[36:37], s[0:1], 0x28
	s_load_dwordx4 s[16:19], s[0:1], 0x30
	s_load_dwordx2 s[20:21], s[0:1], 0x40
	s_and_b32 s3, s2, 15
	s_bfe_u32 s30, s2, 0x30004
	s_lshr_b32 s2, s2, 3
	s_and_b32 s2, s2, 0x1ffffff0
	s_or_b32 s2, s2, s3
	s_mov_b32 s3, 0
	s_lshl_b32 s31, s30, 8
	s_lshl_b64 s[26:27], s[2:3], 19
	s_lshl_b64 s[24:25], s[2:3], 11
	s_lshl_b64 s[38:39], s[2:3], 20
	s_lshl_b32 s43, s30, 17
	s_add_u32 s38, s38, s43
	s_addc_u32 s39, s39, 0
	v_and_b32_e32 v1, 15, v0
	v_lshrrev_b32_e32 v28, 4, v0
	v_lshrrev_b32_e32 v29, 6, v0
	v_lshlrev_b32_e32 v30, 5, v1
	v_lshl_or_b32 v2, v28, 9, v30
	v_bfe_u32 v31, v0, 4, 2
	v_lshl_or_b32 v3, v31, 9, v30
	v_lshl_or_b32 v3, v29, 15, v3
	v_lshlrev_b32_e32 v32, 4, v1
	v_lshl_or_b32 v26, v28, 8, v32
	s_lshl_b32 s43, s30, 16
	v_or_b32_e32 v26, s43, v26
	v_mov_b32_e32 v208, v2
	v_lshlrev_b32_e32 v38, 2, v0
	v_lshlrev_b32_e32 v40, 14, v29
	v_lshlrev_b32_e32 v33, 12, v29
	v_mbcnt_lo_u32_b32 v204, -1, 0
	v_mbcnt_hi_u32_b32 v204, -1, v204
	v_readfirstlane_b32 s28, v33
	v_readfirstlane_b32 s29, v33
	v_mov_b32_e32 v4, 0
	v_mov_b32_e32 v5, 0
	v_mov_b32_e32 v6, 0
	v_mov_b32_e32 v7, 0
	v_mov_b32_e32 v8, 0
	v_mov_b32_e32 v9, 0
	v_mov_b32_e32 v10, 0
	v_mov_b32_e32 v11, 0
	s_mov_b32 s44, 0x3e0293ee
	s_mov_b32 s45, 0x3e0293ee
	s_waitcnt lgkmcnt(0)
	s_add_u32 s12, s4, s26
	s_addc_u32 s13, s5, s27
	s_and_b32 s13, s13, 0xffff
	s_mov_b32 s14, 0x80000
	s_mov_b32 s15, 0x20000
	s_add_u32 s4, s6, s26
	s_addc_u32 s5, s7, s27
	s_and_b32 s5, s5, 0xffff
	s_mov_b32 s6, 0x80000
	s_mov_b32 s7, 0x20000
	s_add_u32 s32, s10, s38
	s_addc_u32 s33, s11, s39
	s_add_u32 s34, s36, s38
	s_addc_u32 s35, s37, s39
	s_add_u32 s40, s22, s38
	s_addc_u32 s41, s23, s39
	s_lshl_b64 s[46:47], s[2:3], 5
	s_add_u32 s10, s16, s46
	s_addc_u32 s11, s17, s47
	s_lshl_b32 s43, s30, 2
	s_add_u32 s46, s10, s43
	s_addc_u32 s47, s11, 0
	s_lshl_b64 s[26:27], s[2:3], 12
	s_add_u32 s26, s18, s26
	s_addc_u32 s27, s19, s27
	s_lshl_b32 s43, s30, 9
	s_add_u32 s26, s26, s43
	s_addc_u32 s27, s27, 0
	global_load_dwordx4 v[42:45], v2, s[32:33] nt
	global_load_dwordx4 v[46:49], v2, s[32:33] offset:16 nt
	s_add_u32 s32, s32, 8192
	s_addc_u32 s33, s33, 0
	global_load_dwordx4 v[50:53], v2, s[32:33] nt
	global_load_dwordx4 v[54:57], v2, s[32:33] offset:16 nt
	s_add_u32 s32, s32, 8192
	s_addc_u32 s33, s33, 0
	global_load_dwordx4 v[58:61], v2, s[32:33] nt
	global_load_dwordx4 v[62:65], v2, s[32:33] offset:16 nt
	s_add_u32 s32, s32, 8192
	s_addc_u32 s33, s33, 0
	global_load_dwordx4 v[66:69], v2, s[32:33] nt
	global_load_dwordx4 v[70:73], v2, s[32:33] offset:16 nt
	s_add_u32 s32, s32, 8192
	s_addc_u32 s33, s33, 0
	global_load_dwordx4 v[74:77], v2, s[32:33] nt
	global_load_dwordx4 v[78:81], v2, s[32:33] offset:16 nt
	s_add_u32 s32, s32, 8192
	s_addc_u32 s33, s33, 0
	global_load_dwordx4 v[82:85], v2, s[32:33] nt
	global_load_dwordx4 v[86:89], v2, s[32:33] offset:16 nt
	s_add_u32 s32, s32, 8192
	s_addc_u32 s33, s33, 0
	global_load_dwordx4 v[90:93], v2, s[32:33] nt
	global_load_dwordx4 v[94:97], v2, s[32:33] offset:16 nt
	s_add_u32 s32, s32, 8192
	s_addc_u32 s33, s33, 0
	global_load_dwordx4 v[98:101], v2, s[32:33] nt
	global_load_dwordx4 v[102:105], v2, s[32:33] offset:16 nt
	s_add_u32 s32, s32, 8192
	s_addc_u32 s33, s33, 0
	global_load_dwordx4 v[248:251], v2, s[32:33] nt
	global_load_dwordx4 v[252:255], v2, s[32:33] offset:16 nt
	s_add_u32 s32, s32, 8192
	s_addc_u32 s33, s33, 0
	global_load_dwordx4 v[106:109], v2, s[34:35] nt
	global_load_dwordx4 v[110:113], v2, s[34:35] offset:16 nt
	s_add_u32 s34, s34, 8192
	s_addc_u32 s35, s35, 0
	global_load_dwordx4 v[114:117], v2, s[34:35] nt
	global_load_dwordx4 v[118:121], v2, s[34:35] offset:16 nt
	s_add_u32 s34, s34, 8192
	s_addc_u32 s35, s35, 0
	global_load_dwordx4 v[122:125], v2, s[34:35] nt
	global_load_dwordx4 v[126:129], v2, s[34:35] offset:16 nt
	s_add_u32 s34, s34, 8192
	s_addc_u32 s35, s35, 0
	global_load_dwordx4 v[130:133], v2, s[34:35] nt
	global_load_dwordx4 v[134:137], v2, s[34:35] offset:16 nt
	s_add_u32 s34, s34, 8192
	s_addc_u32 s35, s35, 0
	global_load_dwordx4 v[138:141], v2, s[34:35] nt
	global_load_dwordx4 v[142:145], v2, s[34:35] offset:16 nt
	s_add_u32 s34, s34, 8192
	s_addc_u32 s35, s35, 0
	global_load_dwordx4 v[146:149], v2, s[34:35] nt
	global_load_dwordx4 v[150:153], v2, s[34:35] offset:16 nt
	s_add_u32 s34, s34, 8192
	s_addc_u32 s35, s35, 0
	global_load_dwordx4 v[154:157], v2, s[34:35] nt
	global_load_dwordx4 v[158:161], v2, s[34:35] offset:16 nt
	s_add_u32 s34, s34, 8192
	s_addc_u32 s35, s35, 0
	global_load_dwordx4 v[162:165], v2, s[34:35] nt
	global_load_dwordx4 v[166:169], v2, s[34:35] offset:16 nt
	s_add_u32 s34, s34, 8192
	s_addc_u32 s35, s35, 0
	global_load_dwordx4 v[170:173], v3, s[40:41] nt
	global_load_dwordx4 v[174:177], v3, s[40:41] offset:16 nt
	s_add_u32 s40, s40, 2048
	s_addc_u32 s41, s41, 0
	global_load_dwordx4 v[178:181], v3, s[40:41] nt
	global_load_dwordx4 v[182:185], v3, s[40:41] offset:16 nt
	s_add_u32 s40, s40, 2048
	s_addc_u32 s41, s41, 0
	global_load_dwordx4 v[186:189], v3, s[40:41] nt
	global_load_dwordx4 v[190:193], v3, s[40:41] offset:16 nt
	s_add_u32 s40, s40, 2048
	s_addc_u32 s41, s41, 0
	global_load_dwordx4 v[194:197], v3, s[40:41] nt
	global_load_dwordx4 v[198:201], v3, s[40:41] offset:16 nt
	s_add_u32 s40, s40, 2048
	s_addc_u32 s41, s41, 0
	s_waitcnt vmcnt(40)
	v_cvt_pk_bf16_f32 v12, v42, v43
	v_cvt_pk_bf16_f32 v13, v44, v45
	v_cvt_pk_bf16_f32 v14, v46, v47
	v_cvt_pk_bf16_f32 v15, v48, v49
	s_mov_b32 s42, 0x0
	buffer_store_dwordx4 v[12:15], v26, s[12:15], s42 offen sc1
	global_load_dwordx4 v[42:45], v3, s[40:41] nt
	global_load_dwordx4 v[46:49], v3, s[40:41] offset:16 nt
	s_add_u32 s40, s40, 2048
	s_addc_u32 s41, s41, 0
	s_waitcnt vmcnt(41)
	v_cvt_pk_bf16_f32 v16, v50, v51
	v_cvt_pk_bf16_f32 v17, v52, v53
	v_cvt_pk_bf16_f32 v18, v54, v55
	v_cvt_pk_bf16_f32 v19, v56, v57
	s_mov_b32 s42, 0x1000
	buffer_store_dwordx4 v[16:19], v26, s[12:15], s42 offen sc1
	global_load_dwordx4 v[50:53], v3, s[40:41] nt
	global_load_dwordx4 v[54:57], v3, s[40:41] offset:16 nt
	s_add_u32 s40, s40, 2048
	s_addc_u32 s41, s41, 0
	s_waitcnt vmcnt(42)
	v_cvt_pk_bf16_f32 v20, v58, v59
	v_cvt_pk_bf16_f32 v21, v60, v61
	v_cvt_pk_bf16_f32 v22, v62, v63
	v_cvt_pk_bf16_f32 v23, v64, v65
	s_mov_b32 s42, 0x2000
	buffer_store_dwordx4 v[20:23], v26, s[12:15], s42 offen sc1
	global_load_dwordx4 v[58:61], v3, s[40:41] nt
	global_load_dwordx4 v[62:65], v3, s[40:41] offset:16 nt
	s_add_u32 s40, s40, 2048
	s_addc_u32 s41, s41, 0
	s_waitcnt vmcnt(43)
	v_cvt_pk_bf16_f32 v12, v66, v67
	v_cvt_pk_bf16_f32 v13, v68, v69
	v_cvt_pk_bf16_f32 v14, v70, v71
	v_cvt_pk_bf16_f32 v15, v72, v73
	s_mov_b32 s42, 0x3000
	buffer_store_dwordx4 v[12:15], v26, s[12:15], s42 offen sc1
	global_load_dwordx4 v[66:69], v3, s[40:41] nt
	global_load_dwordx4 v[70:73], v3, s[40:41] offset:16 nt
	s_add_u32 s40, s40, 2048
	s_addc_u32 s41, s41, 0
	s_waitcnt vmcnt(44)
	v_cvt_pk_bf16_f32 v16, v74, v75
	v_cvt_pk_bf16_f32 v17, v76, v77
	v_cvt_pk_bf16_f32 v18, v78, v79
	v_cvt_pk_bf16_f32 v19, v80, v81
	s_mov_b32 s42, 0x4000
	buffer_store_dwordx4 v[16:19], v26, s[12:15], s42 offen sc1
	global_load_dwordx4 v[74:77], v3, s[40:41] nt
	global_load_dwordx4 v[78:81], v3, s[40:41] offset:16 nt
	s_add_u32 s40, s40, 2048
	s_addc_u32 s41, s41, 0
	s_waitcnt vmcnt(45)
	v_cvt_pk_bf16_f32 v20, v82, v83
	v_cvt_pk_bf16_f32 v21, v84, v85
	v_cvt_pk_bf16_f32 v22, v86, v87
	v_cvt_pk_bf16_f32 v23, v88, v89
	s_mov_b32 s42, 0x5000
	buffer_store_dwordx4 v[20:23], v26, s[12:15], s42 offen sc1
	global_load_dwordx4 v[82:85], v3, s[40:41] nt
	global_load_dwordx4 v[86:89], v3, s[40:41] offset:16 nt
	s_add_u32 s40, s40, 2048
	s_addc_u32 s41, s41, 0
	s_waitcnt vmcnt(46)
	v_cvt_pk_bf16_f32 v12, v90, v91
	v_cvt_pk_bf16_f32 v13, v92, v93
	v_cvt_pk_bf16_f32 v14, v94, v95
	v_cvt_pk_bf16_f32 v15, v96, v97
	s_mov_b32 s42, 0x6000
	buffer_store_dwordx4 v[12:15], v26, s[12:15], s42 offen sc1
	global_load_dwordx4 v[90:93], v3, s[40:41] nt
	global_load_dwordx4 v[94:97], v3, s[40:41] offset:16 nt
	s_add_u32 s40, s40, 2048
	s_addc_u32 s41, s41, 0
	s_waitcnt vmcnt(47)
	v_cvt_pk_bf16_f32 v16, v98, v99
	v_cvt_pk_bf16_f32 v17, v100, v101
	v_cvt_pk_bf16_f32 v18, v102, v103
	v_cvt_pk_bf16_f32 v19, v104, v105
	s_mov_b32 s42, 0x7000
	buffer_store_dwordx4 v[16:19], v26, s[12:15], s42 offen sc1
	global_load_dwordx4 v[98:101], v3, s[40:41] nt
	global_load_dwordx4 v[102:105], v3, s[40:41] offset:16 nt
	s_add_u32 s40, s40, 2048
	s_addc_u32 s41, s41, 0
	s_waitcnt vmcnt(46)
	v_mov_b32_e32 v4, 0
	v_mov_b32_e32 v5, 0
	v_mov_b32_e32 v6, 0
	v_mov_b32_e32 v7, 0
	v_mov_b32_e32 v8, 0
	v_mov_b32_e32 v9, 0
	v_mov_b32_e32 v10, 0
	v_mov_b32_e32 v11, 0
	v_pk_add_f32 v[4:5], v[106:107], v[4:5]
	v_pk_add_f32 v[6:7], v[108:109], v[6:7]
	v_pk_add_f32 v[8:9], v[110:111], v[8:9]
	v_pk_add_f32 v[10:11], v[112:113], v[10:11]
	v_cvt_pk_bf16_f32 v20, v106, v107
	v_cvt_pk_bf16_f32 v21, v108, v109
	v_cvt_pk_bf16_f32 v22, v110, v111
	v_cvt_pk_bf16_f32 v23, v112, v113
	s_mov_b32 s42, 0x0
	buffer_store_dwordx4 v[20:23], v26, s[4:7], s42 offen sc1
	global_load_dwordx4 v[106:109], v3, s[40:41] nt
	global_load_dwordx4 v[110:113], v3, s[40:41] offset:16 nt
	s_add_u32 s40, s40, 2048
	s_addc_u32 s41, s41, 0
	s_waitcnt vmcnt(47)
	v_pk_add_f32 v[4:5], v[114:115], v[4:5]
	v_pk_add_f32 v[6:7], v[116:117], v[6:7]
	v_pk_add_f32 v[8:9], v[118:119], v[8:9]
	v_pk_add_f32 v[10:11], v[120:121], v[10:11]
	v_cvt_pk_bf16_f32 v12, v114, v115
	v_cvt_pk_bf16_f32 v13, v116, v117
	v_cvt_pk_bf16_f32 v14, v118, v119
	v_cvt_pk_bf16_f32 v15, v120, v121
	s_mov_b32 s42, 0x1000
	buffer_store_dwordx4 v[12:15], v26, s[4:7], s42 offen sc1
	global_load_dwordx4 v[114:117], v3, s[40:41] nt
	global_load_dwordx4 v[118:121], v3, s[40:41] offset:16 nt
	s_add_u32 s40, s40, 2048
	s_addc_u32 s41, s41, 0
	s_waitcnt vmcnt(48)
	v_pk_add_f32 v[4:5], v[122:123], v[4:5]
	v_pk_add_f32 v[6:7], v[124:125], v[6:7]
	v_pk_add_f32 v[8:9], v[126:127], v[8:9]
	v_pk_add_f32 v[10:11], v[128:129], v[10:11]
	v_cvt_pk_bf16_f32 v16, v122, v123
	v_cvt_pk_bf16_f32 v17, v124, v125
	v_cvt_pk_bf16_f32 v18, v126, v127
	v_cvt_pk_bf16_f32 v19, v128, v129
	s_mov_b32 s42, 0x2000
	buffer_store_dwordx4 v[16:19], v26, s[4:7], s42 offen sc1
	global_load_dwordx4 v[122:125], v3, s[40:41] nt
	global_load_dwordx4 v[126:129], v3, s[40:41] offset:16 nt
	s_add_u32 s40, s40, 2048
	s_addc_u32 s41, s41, 0
	s_waitcnt vmcnt(49)
	v_pk_add_f32 v[4:5], v[130:131], v[4:5]
	v_pk_add_f32 v[6:7], v[132:133], v[6:7]
	v_pk_add_f32 v[8:9], v[134:135], v[8:9]
	v_pk_add_f32 v[10:11], v[136:137], v[10:11]
	v_cvt_pk_bf16_f32 v20, v130, v131
	v_cvt_pk_bf16_f32 v21, v132, v133
	v_cvt_pk_bf16_f32 v22, v134, v135
	v_cvt_pk_bf16_f32 v23, v136, v137
	s_mov_b32 s42, 0x3000
	buffer_store_dwordx4 v[20:23], v26, s[4:7], s42 offen sc1
	global_load_dwordx4 v[130:133], v3, s[40:41] nt
	global_load_dwordx4 v[134:137], v3, s[40:41] offset:16 nt
	s_add_u32 s40, s40, 2048
	s_addc_u32 s41, s41, 0
	s_waitcnt vmcnt(50)
	v_pk_add_f32 v[4:5], v[138:139], v[4:5]
	v_pk_add_f32 v[6:7], v[140:141], v[6:7]
	v_pk_add_f32 v[8:9], v[142:143], v[8:9]
	v_pk_add_f32 v[10:11], v[144:145], v[10:11]
	v_cvt_pk_bf16_f32 v12, v138, v139
	v_cvt_pk_bf16_f32 v13, v140, v141
	v_cvt_pk_bf16_f32 v14, v142, v143
	v_cvt_pk_bf16_f32 v15, v144, v145
	s_mov_b32 s42, 0x4000
	buffer_store_dwordx4 v[12:15], v26, s[4:7], s42 offen sc1
	s_waitcnt vmcnt(49)
	v_pk_add_f32 v[4:5], v[146:147], v[4:5]
	v_pk_add_f32 v[6:7], v[148:149], v[6:7]
	v_pk_add_f32 v[8:9], v[150:151], v[8:9]
	v_pk_add_f32 v[10:11], v[152:153], v[10:11]
	v_cvt_pk_bf16_f32 v16, v146, v147
	v_cvt_pk_bf16_f32 v17, v148, v149
	v_cvt_pk_bf16_f32 v18, v150, v151
	v_cvt_pk_bf16_f32 v19, v152, v153
	s_mov_b32 s42, 0x5000
	buffer_store_dwordx4 v[16:19], v26, s[4:7], s42 offen sc1
	s_waitcnt vmcnt(48)
	v_pk_add_f32 v[4:5], v[154:155], v[4:5]
	v_pk_add_f32 v[6:7], v[156:157], v[6:7]
	v_pk_add_f32 v[8:9], v[158:159], v[8:9]
	v_pk_add_f32 v[10:11], v[160:161], v[10:11]
	v_cvt_pk_bf16_f32 v20, v154, v155
	v_cvt_pk_bf16_f32 v21, v156, v157
	v_cvt_pk_bf16_f32 v22, v158, v159
	v_cvt_pk_bf16_f32 v23, v160, v161
	s_mov_b32 s42, 0x6000
	buffer_store_dwordx4 v[20:23], v26, s[4:7], s42 offen sc1
	s_waitcnt vmcnt(47)
	v_pk_add_f32 v[4:5], v[162:163], v[4:5]
	v_pk_add_f32 v[6:7], v[164:165], v[6:7]
	v_pk_add_f32 v[8:9], v[166:167], v[8:9]
	v_pk_add_f32 v[10:11], v[168:169], v[10:11]
	v_cvt_pk_bf16_f32 v12, v162, v163
	v_cvt_pk_bf16_f32 v13, v164, v165
	v_cvt_pk_bf16_f32 v14, v166, v167
	v_cvt_pk_bf16_f32 v15, v168, v169
	s_mov_b32 s42, 0x7000
	buffer_store_dwordx4 v[12:15], v26, s[4:7], s42 offen sc1
	s_movk_i32 s0, 0x80
	v_cmp_gt_u32_e64 s[0:1], s0, v0
	s_waitcnt vmcnt(0)
	s_barrier
	v_cmp_eq_u32_e32 vcc, 0, v0
	s_and_saveexec_b64 s[38:39], vcc
	s_cbranch_execz .Lpro_noflag
	v_mov_b32_e32 v12, 0x600df1a6
	v_mov_b32_e32 v13, 0
	global_store_dword v13, v12, s[46:47] sc1
.Lpro_noflag:
	s_or_b64 exec, exec, s[38:39]
	v_lshlrev_b32_e32 v41, 2, v204
	v_and_b32_e32 v41, 28, v41
	global_load_dword v30, v41, s[10:11] sc1
	v_lshrrev_b32_e32 v202, 4, v204
	v_and_b32_e32 v31, 15, v204
	v_xor_b32_e32 v32, v31, v202
	v_xor_b32_e32 v33, 4, v32
	v_lshlrev_b32_e32 v34, 8, v202
	v_or_b32_e32 v35, 0x10000, v40
	v_add_u32_e32 v34, v34, v35
	v_lshl_add_u32 v24, v32, 4, v34
	v_lshl_add_u32 v25, v33, 4, v34
	v_pk_mul_f32 v[170:171], v[170:171], s[44:45] op_sel_hi:[1,0]
	v_pk_mul_f32 v[172:173], v[172:173], s[44:45] op_sel_hi:[1,0]
	v_pk_mul_f32 v[174:175], v[174:175], s[44:45] op_sel_hi:[1,0]
	v_pk_mul_f32 v[176:177], v[176:177], s[44:45] op_sel_hi:[1,0]
	v_cvt_pk_bf16_f32 v12, v170, v171
	v_cvt_pk_bf16_f32 v13, v172, v173
	v_cvt_pk_bf16_f32 v14, v174, v175
	v_cvt_pk_bf16_f32 v15, v176, v177
	ds_write_b128 v24, v[12:15] offset:0
	v_pk_mul_f32 v[178:179], v[178:179], s[44:45] op_sel_hi:[1,0]
	v_pk_mul_f32 v[180:181], v[180:181], s[44:45] op_sel_hi:[1,0]
	v_pk_mul_f32 v[182:183], v[182:183], s[44:45] op_sel_hi:[1,0]
	v_pk_mul_f32 v[184:185], v[184:185], s[44:45] op_sel_hi:[1,0]
	v_cvt_pk_bf16_f32 v16, v178, v179
	v_cvt_pk_bf16_f32 v17, v180, v181
	v_cvt_pk_bf16_f32 v18, v182, v183
	v_cvt_pk_bf16_f32 v19, v184, v185
	ds_write_b128 v25, v[16:19] offset:1024
	v_pk_mul_f32 v[186:187], v[186:187], s[44:45] op_sel_hi:[1,0]
	v_pk_mul_f32 v[188:189], v[188:189], s[44:45] op_sel_hi:[1,0]
	v_pk_mul_f32 v[190:191], v[190:191], s[44:45] op_sel_hi:[1,0]
	v_pk_mul_f32 v[192:193], v[192:193], s[44:45] op_sel_hi:[1,0]
	v_cvt_pk_bf16_f32 v20, v186, v187
	v_cvt_pk_bf16_f32 v21, v188, v189
	v_cvt_pk_bf16_f32 v22, v190, v191
	v_cvt_pk_bf16_f32 v23, v192, v193
	ds_write_b128 v24, v[20:23] offset:2048
	v_pk_mul_f32 v[194:195], v[194:195], s[44:45] op_sel_hi:[1,0]
	v_pk_mul_f32 v[196:197], v[196:197], s[44:45] op_sel_hi:[1,0]
	v_pk_mul_f32 v[198:199], v[198:199], s[44:45] op_sel_hi:[1,0]
	v_pk_mul_f32 v[200:201], v[200:201], s[44:45] op_sel_hi:[1,0]
	v_cvt_pk_bf16_f32 v12, v194, v195
	v_cvt_pk_bf16_f32 v13, v196, v197
	v_cvt_pk_bf16_f32 v14, v198, v199
	v_cvt_pk_bf16_f32 v15, v200, v201
	ds_write_b128 v25, v[12:15] offset:3072
	v_pk_mul_f32 v[42:43], v[42:43], s[44:45] op_sel_hi:[1,0]
	v_pk_mul_f32 v[44:45], v[44:45], s[44:45] op_sel_hi:[1,0]
	v_pk_mul_f32 v[46:47], v[46:47], s[44:45] op_sel_hi:[1,0]
	v_pk_mul_f32 v[48:49], v[48:49], s[44:45] op_sel_hi:[1,0]
	v_cvt_pk_bf16_f32 v16, v42, v43
	v_cvt_pk_bf16_f32 v17, v44, v45
	v_cvt_pk_bf16_f32 v18, v46, v47
	v_cvt_pk_bf16_f32 v19, v48, v49
	ds_write_b128 v24, v[16:19] offset:4096
	v_pk_mul_f32 v[50:51], v[50:51], s[44:45] op_sel_hi:[1,0]
	v_pk_mul_f32 v[52:53], v[52:53], s[44:45] op_sel_hi:[1,0]
	v_pk_mul_f32 v[54:55], v[54:55], s[44:45] op_sel_hi:[1,0]
	v_pk_mul_f32 v[56:57], v[56:57], s[44:45] op_sel_hi:[1,0]
	v_cvt_pk_bf16_f32 v20, v50, v51
	v_cvt_pk_bf16_f32 v21, v52, v53
	v_cvt_pk_bf16_f32 v22, v54, v55
	v_cvt_pk_bf16_f32 v23, v56, v57
	ds_write_b128 v25, v[20:23] offset:5120
	v_pk_mul_f32 v[58:59], v[58:59], s[44:45] op_sel_hi:[1,0]
	v_pk_mul_f32 v[60:61], v[60:61], s[44:45] op_sel_hi:[1,0]
	v_pk_mul_f32 v[62:63], v[62:63], s[44:45] op_sel_hi:[1,0]
	v_pk_mul_f32 v[64:65], v[64:65], s[44:45] op_sel_hi:[1,0]
	v_cvt_pk_bf16_f32 v12, v58, v59
	v_cvt_pk_bf16_f32 v13, v60, v61
	v_cvt_pk_bf16_f32 v14, v62, v63
	v_cvt_pk_bf16_f32 v15, v64, v65
	ds_write_b128 v24, v[12:15] offset:6144
	v_pk_mul_f32 v[66:67], v[66:67], s[44:45] op_sel_hi:[1,0]
	v_pk_mul_f32 v[68:69], v[68:69], s[44:45] op_sel_hi:[1,0]
	v_pk_mul_f32 v[70:71], v[70:71], s[44:45] op_sel_hi:[1,0]
	v_pk_mul_f32 v[72:73], v[72:73], s[44:45] op_sel_hi:[1,0]
	v_cvt_pk_bf16_f32 v16, v66, v67
	v_cvt_pk_bf16_f32 v17, v68, v69
	v_cvt_pk_bf16_f32 v18, v70, v71
	v_cvt_pk_bf16_f32 v19, v72, v73
	ds_write_b128 v25, v[16:19] offset:7168
	v_pk_mul_f32 v[74:75], v[74:75], s[44:45] op_sel_hi:[1,0]
	v_pk_mul_f32 v[76:77], v[76:77], s[44:45] op_sel_hi:[1,0]
	v_pk_mul_f32 v[78:79], v[78:79], s[44:45] op_sel_hi:[1,0]
	v_pk_mul_f32 v[80:81], v[80:81], s[44:45] op_sel_hi:[1,0]
	v_cvt_pk_bf16_f32 v20, v74, v75
	v_cvt_pk_bf16_f32 v21, v76, v77
	v_cvt_pk_bf16_f32 v22, v78, v79
	v_cvt_pk_bf16_f32 v23, v80, v81
	ds_write_b128 v24, v[20:23] offset:8192
	v_pk_mul_f32 v[82:83], v[82:83], s[44:45] op_sel_hi:[1,0]
	v_pk_mul_f32 v[84:85], v[84:85], s[44:45] op_sel_hi:[1,0]
	v_pk_mul_f32 v[86:87], v[86:87], s[44:45] op_sel_hi:[1,0]
	v_pk_mul_f32 v[88:89], v[88:89], s[44:45] op_sel_hi:[1,0]
	v_cvt_pk_bf16_f32 v12, v82, v83
	v_cvt_pk_bf16_f32 v13, v84, v85
	v_cvt_pk_bf16_f32 v14, v86, v87
	v_cvt_pk_bf16_f32 v15, v88, v89
	ds_write_b128 v25, v[12:15] offset:9216
	v_pk_mul_f32 v[90:91], v[90:91], s[44:45] op_sel_hi:[1,0]
	v_pk_mul_f32 v[92:93], v[92:93], s[44:45] op_sel_hi:[1,0]
	v_pk_mul_f32 v[94:95], v[94:95], s[44:45] op_sel_hi:[1,0]
	v_pk_mul_f32 v[96:97], v[96:97], s[44:45] op_sel_hi:[1,0]
	v_cvt_pk_bf16_f32 v16, v90, v91
	v_cvt_pk_bf16_f32 v17, v92, v93
	v_cvt_pk_bf16_f32 v18, v94, v95
	v_cvt_pk_bf16_f32 v19, v96, v97
	ds_write_b128 v24, v[16:19] offset:10240
	v_pk_mul_f32 v[98:99], v[98:99], s[44:45] op_sel_hi:[1,0]
	v_pk_mul_f32 v[100:101], v[100:101], s[44:45] op_sel_hi:[1,0]
	v_pk_mul_f32 v[102:103], v[102:103], s[44:45] op_sel_hi:[1,0]
	v_pk_mul_f32 v[104:105], v[104:105], s[44:45] op_sel_hi:[1,0]
	v_cvt_pk_bf16_f32 v20, v98, v99
	v_cvt_pk_bf16_f32 v21, v100, v101
	v_cvt_pk_bf16_f32 v22, v102, v103
	v_cvt_pk_bf16_f32 v23, v104, v105
	ds_write_b128 v25, v[20:23] offset:11264
	v_pk_mul_f32 v[106:107], v[106:107], s[44:45] op_sel_hi:[1,0]
	v_pk_mul_f32 v[108:109], v[108:109], s[44:45] op_sel_hi:[1,0]
	v_pk_mul_f32 v[110:111], v[110:111], s[44:45] op_sel_hi:[1,0]
	v_pk_mul_f32 v[112:113], v[112:113], s[44:45] op_sel_hi:[1,0]
	v_cvt_pk_bf16_f32 v12, v106, v107
	v_cvt_pk_bf16_f32 v13, v108, v109
	v_cvt_pk_bf16_f32 v14, v110, v111
	v_cvt_pk_bf16_f32 v15, v112, v113
	ds_write_b128 v24, v[12:15] offset:12288
	v_pk_mul_f32 v[114:115], v[114:115], s[44:45] op_sel_hi:[1,0]
	v_pk_mul_f32 v[116:117], v[116:117], s[44:45] op_sel_hi:[1,0]
	v_pk_mul_f32 v[118:119], v[118:119], s[44:45] op_sel_hi:[1,0]
	v_pk_mul_f32 v[120:121], v[120:121], s[44:45] op_sel_hi:[1,0]
	v_cvt_pk_bf16_f32 v16, v114, v115
	v_cvt_pk_bf16_f32 v17, v116, v117
	v_cvt_pk_bf16_f32 v18, v118, v119
	v_cvt_pk_bf16_f32 v19, v120, v121
	ds_write_b128 v25, v[16:19] offset:13312
	v_pk_mul_f32 v[122:123], v[122:123], s[44:45] op_sel_hi:[1,0]
	v_pk_mul_f32 v[124:125], v[124:125], s[44:45] op_sel_hi:[1,0]
	v_pk_mul_f32 v[126:127], v[126:127], s[44:45] op_sel_hi:[1,0]
	v_pk_mul_f32 v[128:129], v[128:129], s[44:45] op_sel_hi:[1,0]
	v_cvt_pk_bf16_f32 v20, v122, v123
	v_cvt_pk_bf16_f32 v21, v124, v125
	v_cvt_pk_bf16_f32 v22, v126, v127
	v_cvt_pk_bf16_f32 v23, v128, v129
	ds_write_b128 v24, v[20:23] offset:14336
	v_pk_mul_f32 v[130:131], v[130:131], s[44:45] op_sel_hi:[1,0]
	v_pk_mul_f32 v[132:133], v[132:133], s[44:45] op_sel_hi:[1,0]
	v_pk_mul_f32 v[134:135], v[134:135], s[44:45] op_sel_hi:[1,0]
	v_pk_mul_f32 v[136:137], v[136:137], s[44:45] op_sel_hi:[1,0]
	v_cvt_pk_bf16_f32 v12, v130, v131
	v_cvt_pk_bf16_f32 v13, v132, v133
	v_cvt_pk_bf16_f32 v14, v134, v135
	v_cvt_pk_bf16_f32 v15, v136, v137
	ds_write_b128 v25, v[12:15] offset:15360
	v_mov_b32_e32 v209, v41
	v_lshrrev_b32_e32 v29, 6, v0
	s_nop 0
	v_readfirstlane_b32 s50, v29
	s_mov_b32 s51, s30
	s_add_i32 s52, s24, s31
	s_mov_b32 s54, s32
	s_mov_b32 s55, s33
	s_lshl_b32 s43, s30, 16
	s_add_i32 s56, s43, 0x8000
	s_mov_b32 s74, s34
	s_mov_b32 s75, s35
	s_mov_b32 s76, s26
	s_mov_b32 s77, s27
	v_mov_b32_e32 v200, v4
	v_mov_b32_e32 v201, v5
	v_mov_b32_e32 v202, v6
	v_mov_b32_e32 v203, v7
	v_mov_b32_e32 v204, v8
	v_mov_b32_e32 v205, v9
	v_mov_b32_e32 v206, v10
	v_mov_b32_e32 v207, v11
	s_add_i32 s61, s28, s43
	s_add_i32 s43, s30, 1
	s_and_b32 s43, s43, 7
	s_lshl_b32 s43, s43, 16
	s_add_i32 s62, s28, s43
	s_add_i32 s43, s30, 7
	s_and_b32 s43, s43, 7
	s_lshl_b32 s43, s43, 16
	s_add_i32 s63, s28, s43
	s_add_i32 s63, s63, 0xc000
	s_add_i32 s58, s62, 0x4000
	s_mov_b32 s57, s62
	s_mov_b32 s59, 0xc000
	s_mov_b32 s60, 0x4000
	s_mov_b32 s64, s10
	s_mov_b32 s65, s11
	s_mov_b32 s66, 0x10000
	s_mov_b32 s67, 0x4000
	s_mov_b32 s68, 0xc000
	s_mov_b32 s69, 0x14000
	s_mov_b32 s70, 0x600df1a6
	s_mov_b32 s71, 0x155500
	s_mov_b32 s72, s46
	s_mov_b32 s73, s47
	s_mov_b32 s22, 0x600df1a6
	s_mov_b32 s23, 0x10000
	s_waitcnt vmcnt(0) lgkmcnt(0)
	v_cmp_eq_u32_e32 vcc, s22, v30
	s_cmp_eq_u64 vcc, exec
	s_cbranch_scc0 .LBB0_27
.LBB0_11:
	v_bfe_u32 v3, v0, 5, 1
	v_lshlrev_b32_e32 v4, 8, v0
	v_and_b32_e32 v4, 0x1f00, v4
	v_and_b32_e32 v5, 7, v0
	v_bitop3_b32 v6, v3, v0, 7 bitop3:0x78
	v_lshl_or_b32 v64, v6, 4, v4
	v_bitop3_b32 v6, v3, v5, 2 bitop3:0x36
	v_lshl_or_b32 v65, v6, 4, v4
	v_bitop3_b32 v6, v3, v5, 4 bitop3:0x36
	v_bitop3_b32 v5, v3, v5, 6 bitop3:0x36
	v_lshl_or_b32 v66, v6, 4, v4
	v_lshl_or_b32 v67, v5, 4, v4
	v_and_b32_e32 v4, 3, v0
	v_lshlrev_b32_e32 v6, 4, v0
	v_lshlrev_b32_e32 v5, 3, v4
	v_and_b32_e32 v6, 0xc0, v6
	v_lshlrev_b32_e32 v8, 1, v0
	v_lshlrev_b32_e32 v9, 8, v3
	v_bfe_u32 v7, v0, 4, 2
	v_and_b32_e32 v8, 32, v8
	v_or3_b32 v5, v5, v9, v6
	s_mov_b32 s0, 0x8000
	v_or3_b32 v184, v5, v8, s0
	v_lshlrev_b32_e32 v5, 8, v7
	v_xor_b32_e32 v6, v7, v1
	s_cmp_lg_u32 0, -1
	v_lshl_or_b32 v222, v6, 4, v5
	v_bitop3_b32 v1, v7, v1, 4 bitop3:0x36
	s_mov_b32 m0, s29
	s_nop 0
	buffer_load_dwordx4 v222, s[12:15], s61 offen lds
	s_cselect_b32 s17, 0, 0
	v_lshl_or_b32 v223, v1, 4, v5
	s_add_i32 s20, s29, 0x400
	s_add_i32 s0, s61, 0x400
	s_mov_b32 m0, s20
	s_nop 0
	buffer_load_dwordx4 v223, s[12:15], s0 offen lds
	v_lshlrev_b32_e32 v0, 6, v0
	s_add_i32 s21, s29, 0x800
	s_add_i32 s0, s61, 0x800
	s_mov_b32 m0, s21
	s_nop 0
	buffer_load_dwordx4 v222, s[12:15], s0 offen lds
	v_and_b32_e32 v0, 0x700, v0
	v_lshlrev_b32_e32 v1, 6, v3
	v_lshlrev_b32_e32 v3, 4, v4
	s_add_i32 s22, s29, 0xc00
	s_add_i32 s1, s61, 0xc00
	s_mov_b32 m0, s22
	s_nop 0
	buffer_load_dwordx4 v223, s[12:15], s1 offen lds
	v_or3_b32 v196, v0, v1, v3
	s_add_i32 s2, s29, 0x8000
	s_mov_b32 m0, s2
	s_nop 0
	buffer_load_dwordx4 v196, s[4:7], s61 offen lds
	s_add_i32 s1, s2, 0x400
	s_add_i32 s3, s61, 0x80
	s_mov_b32 m0, s1
	s_nop 0
	buffer_load_dwordx4 v196, s[4:7], s3 offen lds
	s_add_i32 s1, s2, 0x800
	s_mov_b32 m0, s1
	s_nop 0
	buffer_load_dwordx4 v196, s[4:7], s0 offen lds
	s_add_i32 s0, s2, 0xc00
	s_add_i32 s1, s61, 0x880
	s_mov_b32 m0, s0
	s_nop 0
	buffer_load_dwordx4 v196, s[4:7], s1 offen lds
	s_add_i32 s3, s29, 0x4000
	s_add_i32 s19, s61, 0x4000
	s_mov_b32 m0, s3
	s_nop 0
	buffer_load_dwordx4 v222, s[12:15], s19 offen lds
	v_or_b32_e32 v2, 0x10000, v40
	v_add_u32_e32 v218, s17, v64
	v_add_u32_e32 v219, s17, v65
	v_add_u32_e32 v220, s17, v66
	v_add_u32_e32 v221, s17, v67
	s_add_i32 s10, s29, 0x4400
	s_add_i32 s0, s61, 0x4400
	s_mov_b32 m0, s10
	s_nop 0
	buffer_load_dwordx4 v223, s[12:15], s0 offen lds
	s_add_i32 s11, s29, 0x4800
	s_add_i32 s18, s61, 0x4800
	s_mov_b32 m0, s11
	s_nop 0
	buffer_load_dwordx4 v222, s[12:15], s18 offen lds
	v_add_u32_e32 v32, v2, v218
	v_add_u32_e32 v33, v2, v219
	v_add_u32_e32 v34, v2, v220
	v_add_u32_e32 v35, v2, v221
	s_add_i32 s16, s29, 0x4c00
	s_add_i32 s0, s61, 0x4c00
	s_mov_b32 m0, s16
	s_nop 0
	buffer_load_dwordx4 v223, s[12:15], s0 offen lds
	v_add_u32_e32 v212, s17, v184
	ds_read_b128 v[0:3], v32 offset:0
	ds_read_b128 v[4:7], v33 offset:0
	ds_read_b128 v[8:11], v34 offset:0
	ds_read_b128 v[12:15], v35 offset:0
	ds_read_b128 v[16:19], v32 offset:128
	ds_read_b128 v[20:23], v33 offset:128
	ds_read_b128 v[24:27], v34 offset:128
	ds_read_b128 v[28:31], v35 offset:128
	s_waitcnt lgkmcnt(0)
	v_accvgpr_write_b32 a[128], v0
	v_accvgpr_write_b32 a[129], v1
	v_accvgpr_write_b32 a[130], v2
	v_accvgpr_write_b32 a[131], v3
	v_accvgpr_write_b32 a[132], v4
	v_accvgpr_write_b32 a[133], v5
	v_accvgpr_write_b32 a[134], v6
	v_accvgpr_write_b32 a[135], v7
	v_accvgpr_write_b32 a[136], v8
	v_accvgpr_write_b32 a[137], v9
	v_accvgpr_write_b32 a[138], v10
	v_accvgpr_write_b32 a[139], v11
	v_accvgpr_write_b32 a[140], v12
	v_accvgpr_write_b32 a[141], v13
	v_accvgpr_write_b32 a[142], v14
	v_accvgpr_write_b32 a[143], v15
	v_accvgpr_write_b32 a[144], v16
	v_accvgpr_write_b32 a[145], v17
	v_accvgpr_write_b32 a[146], v18
	v_accvgpr_write_b32 a[147], v19
	v_accvgpr_write_b32 a[148], v20
	v_accvgpr_write_b32 a[149], v21
	v_accvgpr_write_b32 a[150], v22
	v_accvgpr_write_b32 a[151], v23
	v_accvgpr_write_b32 a[152], v24
	v_accvgpr_write_b32 a[153], v25
	v_accvgpr_write_b32 a[154], v26
	v_accvgpr_write_b32 a[155], v27
	v_accvgpr_write_b32 a[156], v28
	v_accvgpr_write_b32 a[157], v29
	v_accvgpr_write_b32 a[158], v30
	v_accvgpr_write_b32 a[159], v31
	ds_read_b128 v[0:3], v32 offset:8192
	ds_read_b128 v[4:7], v33 offset:8192
	ds_read_b128 v[8:11], v34 offset:8192
	ds_read_b128 v[12:15], v35 offset:8192
	ds_read_b128 v[16:19], v32 offset:8320
	ds_read_b128 v[20:23], v33 offset:8320
	ds_read_b128 v[24:27], v34 offset:8320
	ds_read_b128 v[28:31], v35 offset:8320
	s_waitcnt lgkmcnt(0)
	v_accvgpr_write_b32 a[160], v0
	v_accvgpr_write_b32 a[161], v1
	v_accvgpr_write_b32 a[162], v2
	v_accvgpr_write_b32 a[163], v3
	v_accvgpr_write_b32 a[164], v4
	v_accvgpr_write_b32 a[165], v5
	v_accvgpr_write_b32 a[166], v6
	v_accvgpr_write_b32 a[167], v7
	v_accvgpr_write_b32 a[168], v8
	v_accvgpr_write_b32 a[169], v9
	v_accvgpr_write_b32 a[170], v10
	v_accvgpr_write_b32 a[171], v11
	v_accvgpr_write_b32 a[172], v12
	v_accvgpr_write_b32 a[173], v13
	v_accvgpr_write_b32 a[174], v14
	v_accvgpr_write_b32 a[175], v15
	v_accvgpr_write_b32 a[176], v16
	v_accvgpr_write_b32 a[177], v17
	v_accvgpr_write_b32 a[178], v18
	v_accvgpr_write_b32 a[179], v19
	v_accvgpr_write_b32 a[180], v20
	v_accvgpr_write_b32 a[181], v21
	v_accvgpr_write_b32 a[182], v22
	v_accvgpr_write_b32 a[183], v23
	v_accvgpr_write_b32 a[184], v24
	v_accvgpr_write_b32 a[185], v25
	v_accvgpr_write_b32 a[186], v26
	v_accvgpr_write_b32 a[187], v27
	v_accvgpr_write_b32 a[188], v28
	v_accvgpr_write_b32 a[189], v29
	v_accvgpr_write_b32 a[190], v30
	v_accvgpr_write_b32 a[191], v31
	s_waitcnt vmcnt(0) lgkmcnt(0)
	s_barrier
	s_nop 0
	ds_read_b128 a[192:195], v218 offset:0
	s_nop 0
	ds_read_b128 a[196:199], v219 offset:0
	ds_read_b128 a[200:203], v220 offset:0
	ds_read_b128 a[204:207], v221 offset:0
	ds_read_b128 a[208:211], v218 offset:128
	ds_read_b128 a[212:215], v219 offset:128
	ds_read_b128 a[216:219], v220 offset:128
	ds_read_b128 a[220:223], v221 offset:128
	ds_read_b128 a[224:227], v218 offset:8192
	ds_read_b128 a[228:231], v219 offset:8192
	ds_read_b128 a[232:235], v220 offset:8192
	ds_read_b128 a[236:239], v221 offset:8192
	ds_read_b128 a[240:243], v218 offset:8320
	ds_read_b128 a[244:247], v219 offset:8320
	ds_read_b128 a[248:251], v220 offset:8320
	ds_read_b128 a[252:255], v221 offset:8320
	s_waitcnt lgkmcnt(0)
	v_mfma_f32_32x32x16_bf16 v[48:63], a[192:195], a[128:131], 0
	v_mfma_f32_32x32x16_bf16 v[32:47], a[192:195], a[160:163], 0
	v_mfma_f32_32x32x16_bf16 v[0:15], a[224:227], a[128:131], 0
	v_mfma_f32_32x32x16_bf16 v[16:31], a[224:227], a[160:163], 0
	v_mfma_f32_32x32x16_bf16 v[48:63], a[196:199], a[132:135], v[48:63]
	v_mfma_f32_32x32x16_bf16 v[32:47], a[196:199], a[164:167], v[32:47]
	v_mfma_f32_32x32x16_bf16 v[0:15], a[228:231], a[132:135], v[0:15]
	v_mfma_f32_32x32x16_bf16 v[16:31], a[228:231], a[164:167], v[16:31]
	v_mfma_f32_32x32x16_bf16 v[48:63], a[200:203], a[136:139], v[48:63]
	v_mfma_f32_32x32x16_bf16 v[32:47], a[200:203], a[168:171], v[32:47]
	v_mfma_f32_32x32x16_bf16 v[0:15], a[232:235], a[136:139], v[0:15]
	v_mfma_f32_32x32x16_bf16 v[16:31], a[232:235], a[168:171], v[16:31]
	v_mfma_f32_32x32x16_bf16 v[48:63], a[204:207], a[140:143], v[48:63]
	v_mfma_f32_32x32x16_bf16 v[32:47], a[204:207], a[172:175], v[32:47]
	v_mfma_f32_32x32x16_bf16 v[0:15], a[236:239], a[140:143], v[0:15]
	v_mfma_f32_32x32x16_bf16 v[16:31], a[236:239], a[172:175], v[16:31]
	v_mfma_f32_32x32x16_bf16 v[48:63], a[208:211], a[144:147], v[48:63]
	s_mov_b32 s27, s29
	v_mfma_f32_32x32x16_bf16 v[32:47], a[208:211], a[176:179], v[32:47]
	s_add_i32 s0, s62, 0x0
	s_mov_b32 s30, s0
	v_mfma_f32_32x32x16_bf16 v[0:15], a[240:243], a[144:147], v[0:15]
	s_mov_b32 s31, s20
	v_mfma_f32_32x32x16_bf16 v[16:31], a[240:243], a[176:179], v[16:31]
	s_add_i32 s33, s62, 0x400
	v_mfma_f32_32x32x16_bf16 v[48:63], a[212:215], a[148:151], v[48:63]
	s_mov_b32 s34, s21
	v_mfma_f32_32x32x16_bf16 v[32:47], a[212:215], a[180:183], v[32:47]
	s_add_i32 s1, s62, 0x800
	s_mov_b32 s35, s1
	v_mfma_f32_32x32x16_bf16 v[0:15], a[244:247], a[148:151], v[0:15]
	s_mov_b32 s36, s22
	v_mfma_f32_32x32x16_bf16 v[16:31], a[244:247], a[180:183], v[16:31]
	s_add_i32 s37, s62, 0xc00
	v_mfma_f32_32x32x16_bf16 v[48:63], a[216:219], a[152:155], v[48:63]
	s_add_i32 s23, s29, 0xc000
	s_mov_b32 s38, s23
	v_mfma_f32_32x32x16_bf16 v[32:47], a[216:219], a[184:187], v[32:47]
	v_mfma_f32_32x32x16_bf16 v[0:15], a[248:251], a[152:155], v[0:15]
	s_add_i32 s24, s29, 0xc400
	s_mov_b32 s39, s24
	v_mfma_f32_32x32x16_bf16 v[16:31], a[248:251], a[184:187], v[16:31]
	s_add_i32 s40, s61, 0x4080
	v_mfma_f32_32x32x16_bf16 v[48:63], a[220:223], a[156:159], v[48:63]
	s_add_i32 s25, s29, 0xc800
	s_mov_b32 s41, s25
	v_mfma_f32_32x32x16_bf16 v[32:47], a[220:223], a[188:191], v[32:47]
	v_mfma_f32_32x32x16_bf16 v[0:15], a[252:255], a[156:159], v[0:15]
	s_add_i32 s26, s29, 0xcc00
	s_mov_b32 s42, s26
	v_mfma_f32_32x32x16_bf16 v[16:31], a[252:255], a[188:191], v[16:31]
	s_add_i32 s43, s61, 0x4880
	s_nop 0
	s_nop 4
	s_waitcnt vmcnt(0) lgkmcnt(0)
	s_barrier
	s_nop 0
	s_mov_b32 m0, s27
	s_nop 0
	buffer_load_dwordx4 v222, s[12:15], s30 offen lds
	s_mov_b32 m0, s31
	s_nop 0
	buffer_load_dwordx4 v223, s[12:15], s33 offen lds
	s_addk_i32 s17, 0x4000
	v_add_u32_e32 v217, s17, v64
	ds_read_b128 a[192:195], v217 offset:0
	s_mov_b32 m0, s34
	s_nop 0
	buffer_load_dwordx4 v222, s[12:15], s35 offen lds
	v_add_u32_e32 v199, s17, v65
	ds_read_b128 a[196:199], v199 offset:0
	s_mov_b32 m0, s36
	s_nop 0
	buffer_load_dwordx4 v223, s[12:15], s37 offen lds
	v_add_u32_e32 v198, s17, v66
	ds_read_b128 a[200:203], v198 offset:0
	s_mov_b32 m0, s38
	s_nop 0
	buffer_load_dwordx4 v196, s[4:7], s19 offen lds
	v_add_u32_e32 v197, s17, v67
	ds_read_b128 a[204:207], v197 offset:0
	s_mov_b32 m0, s39
	s_nop 0
	buffer_load_dwordx4 v196, s[4:7], s40 offen lds
	ds_read_b128 a[208:211], v217 offset:128
	s_mov_b32 m0, s41
	s_nop 0
	buffer_load_dwordx4 v196, s[4:7], s18 offen lds
	ds_read_b128 a[212:215], v199 offset:128
	s_mov_b32 m0, s42
	s_nop 0
	buffer_load_dwordx4 v196, s[4:7], s43 offen lds
	ds_read_b128 a[216:219], v198 offset:128
	ds_read_b128 a[220:223], v197 offset:128
	v_cvt_pk_bf16_f32 v248, v248, v249
	v_cvt_pk_bf16_f32 v249, v250, v251
	v_cvt_pk_bf16_f32 v250, v252, v253
	v_cvt_pk_bf16_f32 v251, v254, v255
	v_lshrrev_b32_e32 v252, 1, v208
	buffer_store_dwordx4 v[248:251], v252, s[12:15], s56 offen sc1
	s_nop 1
	global_load_dwordx4 v[248:251], v208, s[74:75] nt
	global_load_dwordx4 v[252:255], v208, s[74:75] offset:16 nt
	s_add_u32 s74, s74, 0x2000
	s_addc_u32 s75, s75, 0
	v_max3_f32 v64, v48, v49, v0
	v_max3_f32 v65, v50, v51, v1
	v_max3_f32 v64, v64, v2, v3
	ds_read_b128 a[224:227], v217 offset:8192
	v_max3_f32 v64, v64, v52, v53
	v_max3_f32 v65, v65, v54, v55
	v_max3_f32 v64, v64, v4, v5
	v_max3_f32 v65, v65, v6, v7
	ds_read_b128 a[228:231], v199 offset:8192
	v_max3_f32 v64, v64, v56, v57
	v_max3_f32 v65, v65, v58, v59
	v_max3_f32 v64, v64, v8, v9
	v_max3_f32 v65, v65, v10, v11
	ds_read_b128 a[232:235], v198 offset:8192
	v_max3_f32 v64, v64, v60, v61
	v_max3_f32 v65, v65, v62, v63
	v_max3_f32 v64, v64, v12, v13
	v_max3_f32 v65, v65, v14, v15
	ds_read_b128 a[236:239], v197 offset:8192
	v_max3_f32 v66, v32, v33, v16
	v_max3_f32 v67, v34, v35, v17
	v_max3_f32 v66, v66, v18, v19
	ds_read_b128 a[240:243], v217 offset:8320
	v_max3_f32 v66, v66, v36, v37
	v_max3_f32 v67, v67, v38, v39
	v_max3_f32 v66, v66, v20, v21
	v_max3_f32 v67, v67, v22, v23
	ds_read_b128 a[244:247], v199 offset:8320
	v_max3_f32 v66, v66, v40, v41
	v_max3_f32 v67, v67, v42, v43
	v_max3_f32 v66, v66, v24, v25
	v_max3_f32 v67, v67, v26, v27
	ds_read_b128 a[248:251], v198 offset:8320
	v_max3_f32 v66, v66, v44, v45
	v_max3_f32 v67, v67, v46, v47
	v_max3_f32 v66, v66, v28, v29
	v_max3_f32 v67, v67, v30, v31
	ds_read_b128 a[252:255], v197 offset:8320
	v_max_f32_e32 v64, v64, v65
	v_mov_b32_e32 v65, v64
	s_nop 1
	v_permlane32_swap_b32_e32 v64, v65
	v_max_f32_e32 v214, v64, v65
	v_max_f32_e32 v64, v66, v67
	v_mov_b32_e32 v65, v64
	s_nop 1
	v_permlane32_swap_b32_e32 v64, v65
	v_max_f32_e32 v213, v64, v65
	v_sub_f32_e32 v64, v0, v214
	v_mbcnt_lo_u32_b32 v0, -1, 0
	v_mbcnt_hi_u32_b32 v0, -1, v0
	v_sub_f32_e32 v65, v1, v214
	v_xor_b32_e32 v1, 0x80000000, v214
	v_cmp_gt_u32_e32 vcc, 32, v0
	v_sub_f32_e32 v128, v2, v214
	v_sub_f32_e32 v129, v3, v214
	v_sub_f32_e32 v130, v4, v214
	v_sub_f32_e32 v131, v5, v214
	v_sub_f32_e32 v132, v6, v214
	v_sub_f32_e32 v133, v7, v214
	v_sub_f32_e32 v134, v8, v214
	v_sub_f32_e32 v135, v9, v214
	v_sub_f32_e32 v136, v10, v214
	v_sub_f32_e32 v137, v11, v214
	v_sub_f32_e32 v138, v12, v214
	v_sub_f32_e32 v139, v13, v214
	v_sub_f32_e32 v140, v14, v214
	v_sub_f32_e32 v141, v15, v214
	v_sub_f32_e32 v142, v16, v213
	v_mov_b32_e32 v211, 1.0
	v_sub_f32_e32 v143, v17, v213
	v_xor_b32_e32 v17, 0x80000000, v213
	v_cndmask_b32_e64 v0, 0, 1.0, vcc
	s_nop 1
	v_mfma_f32_32x32x2_f32 v[0:15], v0, v1, 0
	v_mbcnt_lo_u32_b32 v16, -1, 0
	v_mbcnt_hi_u32_b32 v16, -1, v16
	v_sub_f32_e32 v48, v48, v214
	v_sub_f32_e32 v49, v49, v214
	v_sub_f32_e32 v50, v50, v214
	v_sub_f32_e32 v51, v51, v214
	v_sub_f32_e32 v52, v52, v214
	v_sub_f32_e32 v53, v53, v214
	v_sub_f32_e32 v54, v54, v214
	v_sub_f32_e32 v55, v55, v214
	v_sub_f32_e32 v56, v56, v214
	v_sub_f32_e32 v57, v57, v214
	v_sub_f32_e32 v58, v58, v214
	v_sub_f32_e32 v59, v59, v214
	v_sub_f32_e32 v60, v60, v214
	v_sub_f32_e32 v61, v61, v214
	v_sub_f32_e32 v62, v62, v214
	v_sub_f32_e32 v63, v63, v214
	v_sub_f32_e32 v32, v32, v213
	v_sub_f32_e32 v33, v33, v213
	v_sub_f32_e32 v34, v34, v213
	v_cmp_gt_u32_e32 vcc, 32, v16
	v_sub_f32_e32 v35, v35, v213
	v_sub_f32_e32 v36, v36, v213
	v_sub_f32_e32 v37, v37, v213
	v_sub_f32_e32 v38, v38, v213
	v_sub_f32_e32 v39, v39, v213
	v_sub_f32_e32 v40, v40, v213
	v_sub_f32_e32 v41, v41, v213
	v_sub_f32_e32 v42, v42, v213
	v_sub_f32_e32 v43, v43, v213
	v_sub_f32_e32 v44, v44, v213
	v_sub_f32_e32 v45, v45, v213
	v_sub_f32_e32 v46, v46, v213
	v_sub_f32_e32 v47, v47, v213
	v_sub_f32_e32 v144, v18, v213
	v_sub_f32_e32 v145, v19, v213
	v_sub_f32_e32 v146, v20, v213
	v_sub_f32_e32 v147, v21, v213
	v_sub_f32_e32 v183, v22, v213
	v_sub_f32_e32 v194, v23, v213
	v_cndmask_b32_e64 v16, 0, 1.0, vcc
	v_sub_f32_e32 v195, v24, v213
	v_sub_f32_e32 v215, v25, v213
	v_sub_f32_e32 v216, v26, v213
	v_sub_f32_e32 v224, v27, v213
	v_sub_f32_e32 v225, v28, v213
	v_sub_f32_e32 v226, v29, v213
	v_sub_f32_e32 v229, v30, v213
	v_sub_f32_e32 v230, v31, v213
	v_mfma_f32_32x32x2_f32 v[16:31], v16, v17, 0
	v_exp_f32_e32 v112, v48
	v_exp_f32_e32 v113, v49
	v_exp_f32_e32 v114, v50
	v_exp_f32_e32 v115, v51
	v_mov_b32_e32 v193, 0
	v_add_f32_e32 v48, v193, v112
	v_add_f32_e32 v49, v193, v113
	v_exp_f32_e32 v116, v52
	v_exp_f32_e32 v117, v53
	v_exp_f32_e32 v118, v54
	v_add_f32_e32 v48, v48, v114
	v_add_f32_e32 v49, v49, v115
	v_exp_f32_e32 v119, v55
	v_exp_f32_e32 v120, v56
	v_add_f32_e32 v48, v48, v116
	v_add_f32_e32 v49, v49, v117
	v_add_f32_e32 v48, v48, v118
	v_exp_f32_e32 v121, v57
	v_exp_f32_e32 v122, v58
	v_exp_f32_e32 v123, v59
	v_add_f32_e32 v49, v49, v119
	v_add_f32_e32 v48, v48, v120
	v_exp_f32_e32 v124, v60
	v_exp_f32_e32 v125, v61
	v_add_f32_e32 v49, v49, v121
	v_add_f32_e32 v48, v48, v122
	v_add_f32_e32 v49, v49, v123
	v_exp_f32_e32 v126, v62
	v_exp_f32_e32 v127, v63
	v_exp_f32_e32 v96, v32
	v_add_f32_e32 v32, v48, v124
	v_add_f32_e32 v48, v49, v125
	v_exp_f32_e32 v97, v33
	v_exp_f32_e32 v98, v34
	v_add_f32_e32 v231, v32, v126
	v_add_f32_e32 v232, v48, v127
	v_add_f32_e32 v32, v193, v96
	v_exp_f32_e32 v99, v35
	v_exp_f32_e32 v100, v36
	v_exp_f32_e32 v101, v37
	v_add_f32_e32 v33, v193, v97
	v_add_f32_e32 v32, v32, v98
	v_exp_f32_e32 v102, v38
	v_exp_f32_e32 v103, v39
	v_add_f32_e32 v33, v33, v99
	v_add_f32_e32 v32, v32, v100
	v_add_f32_e32 v33, v33, v101
	v_exp_f32_e32 v104, v40
	v_exp_f32_e32 v105, v41
	v_exp_f32_e32 v106, v42
	v_add_f32_e32 v32, v32, v102
	v_add_f32_e32 v33, v33, v103
	v_exp_f32_e32 v107, v43
	v_exp_f32_e32 v108, v44
	v_add_f32_e32 v32, v32, v104
	v_add_f32_e32 v33, v33, v105
	v_add_f32_e32 v32, v32, v106
	v_exp_f32_e32 v109, v45
	v_exp_f32_e32 v110, v46
	v_exp_f32_e32 v111, v47
	v_add_f32_e32 v33, v33, v107
	v_add_f32_e32 v32, v32, v108
	s_waitcnt lgkmcnt(0)
	v_add_f32_e32 v33, v33, v109
	v_add_f32_e32 v233, v32, v110
	v_add_f32_e32 v234, v33, v111
	v_mfma_f32_32x32x16_bf16 v[80:95], a[192:195], a[128:131], v[0:15]
	ds_read_b64_tr_b16 v[160:161], v212 offset:0
	v_exp_f32_e32 v235, v64
	v_exp_f32_e32 v236, v65
	v_cvt_pk_bf16_f32 v152, v112, v113
	v_mfma_f32_32x32x16_bf16 v[64:79], a[192:195], a[160:163], v[16:31]
	ds_read_b64_tr_b16 v[162:163], v212 offset:0x800
	v_exp_f32_e32 v237, v128
	v_exp_f32_e32 v238, v129
	v_cvt_pk_bf16_f32 v153, v114, v115
	v_exp_f32_e32 v115, v130
	v_mfma_f32_32x32x16_bf16 v[48:63], a[224:227], a[128:131], v[0:15]
	ds_read_b64_tr_b16 v[172:173], v212 offset:0x200
	v_exp_f32_e32 v239, v131
	v_cvt_pk_bf16_f32 v154, v116, v117
	v_mfma_f32_32x32x16_bf16 v[32:47], a[224:227], a[160:163], v[16:31]
	ds_read_b64_tr_b16 v[174:175], v212 offset:0xa00
	ds_read_b64_tr_b16 v[168:169], v212 offset:0x400
	v_exp_f32_e32 v240, v132
	v_exp_f32_e32 v241, v133
	v_cvt_pk_bf16_f32 v155, v118, v119
	v_exp_f32_e32 v185, v134
	v_exp_f32_e32 v186, v135
	v_mfma_f32_32x32x16_bf16 v[80:95], a[196:199], a[132:135], v[80:95]
	ds_read_b64_tr_b16 v[170:171], v212 offset:0xc00
	v_cvt_pk_bf16_f32 v128, v120, v121
	v_exp_f32_e32 v187, v136
	v_exp_f32_e32 v188, v137
	v_mfma_f32_32x32x16_bf16 v[64:79], a[196:199], a[164:167], v[64:79]
	ds_read_b64_tr_b16 v[176:177], v212 offset:0x600
	v_cvt_pk_bf16_f32 v129, v122, v123
	v_exp_f32_e32 v189, v138
	v_exp_f32_e32 v190, v139
	v_mfma_f32_32x32x16_bf16 v[48:63], a[228:231], a[132:135], v[48:63]
	ds_read_b64_tr_b16 v[178:179], v212 offset:0xe00
	v_cvt_pk_bf16_f32 v130, v124, v125
	v_mfma_f32_32x32x16_bf16 v[32:47], a[228:231], a[164:167], v[32:47]
	ds_read_b64_tr_b16 v[164:165], v212 offset:0x1000
	v_exp_f32_e32 v191, v140
	v_exp_f32_e32 v192, v141
	ds_read_b64_tr_b16 v[166:167], v212 offset:0x1800
	v_cvt_pk_bf16_f32 v131, v126, v127
	v_exp_f32_e32 v141, v142
	v_exp_f32_e32 v142, v143
	v_mfma_f32_32x32x16_bf16 v[80:95], a[200:203], a[136:139], v[80:95]
	ds_read_b64_tr_b16 v[156:157], v212 offset:0x1200
	v_cvt_pk_bf16_f32 v180, v96, v97
	v_exp_f32_e32 v143, v144
	v_mfma_f32_32x32x16_bf16 v[64:79], a[200:203], a[168:171], v[64:79]
	ds_read_b64_tr_b16 v[158:159], v212 offset:0x1a00
	v_exp_f32_e32 v242, v145
	v_cvt_pk_bf16_f32 v181, v98, v99
	v_mfma_f32_32x32x16_bf16 v[48:63], a[232:235], a[136:139], v[48:63]
	ds_read_b64_tr_b16 v[148:149], v212 offset:0x1400
	v_exp_f32_e32 v243, v146
	v_exp_f32_e32 v244, v147
	v_cvt_pk_bf16_f32 v182, v100, v101
	v_mfma_f32_32x32x16_bf16 v[32:47], a[232:235], a[168:171], v[32:47]
	ds_read_b64_tr_b16 v[150:151], v212 offset:0x1c00
	ds_read_b64_tr_b16 v[136:137], v212 offset:0x1600
	v_exp_f32_e32 v245, v183
	v_exp_f32_e32 v246, v194
	v_cvt_pk_bf16_f32 v183, v102, v103
	v_exp_f32_e32 v194, v195
	v_exp_f32_e32 v195, v215
	v_mfma_f32_32x32x16_bf16 v[80:95], a[204:207], a[140:143], v[80:95]
	ds_read_b64_tr_b16 v[138:139], v212 offset:0x1e00
	v_cvt_pk_bf16_f32 v144, v104, v105
	v_exp_f32_e32 v215, v216
	v_exp_f32_e32 v224, v224
	v_mfma_f32_32x32x16_bf16 v[64:79], a[204:207], a[172:175], v[64:79]
	ds_read_b64_tr_b16 v[132:133], v212 offset:0x2000
	v_cvt_pk_bf16_f32 v145, v106, v107
	v_exp_f32_e32 v227, v225
	v_exp_f32_e32 v228, v226
	v_mfma_f32_32x32x16_bf16 v[48:63], a[236:239], a[140:143], v[48:63]
	ds_read_b64_tr_b16 v[134:135], v212 offset:0x2800
	v_cvt_pk_bf16_f32 v146, v108, v109
	v_mfma_f32_32x32x16_bf16 v[32:47], a[236:239], a[172:175], v[32:47]
	ds_read_b64_tr_b16 v[124:125], v212 offset:0x2200
	v_exp_f32_e32 v229, v229
	v_exp_f32_e32 v230, v230
	ds_read_b64_tr_b16 v[126:127], v212 offset:0x2a00
	v_cvt_pk_bf16_f32 v147, v110, v111
	s_mov_b32 s27, s3
	v_mfma_f32_32x32x16_bf16 v[80:95], a[208:211], a[144:147], v[80:95]
	ds_read_b64_tr_b16 v[120:121], v212 offset:0x2400
	v_cvt_pk_bf16_f32 v112, v235, v236
	v_add_f32_e32 v96, v231, v235
	v_add_f32_e32 v97, v232, v236
	s_add_i32 s30, s62, 0x4000
	v_mfma_f32_32x32x16_bf16 v[64:79], a[208:211], a[176:179], v[64:79]
	ds_read_b64_tr_b16 v[122:123], v212 offset:0x2c00
	v_cvt_pk_bf16_f32 v113, v237, v238
	v_add_f32_e32 v96, v96, v237
	v_add_f32_e32 v97, v97, v238
	s_mov_b32 s31, s10
	v_mfma_f32_32x32x16_bf16 v[48:63], a[240:243], a[144:147], v[48:63]
	ds_read_b64_tr_b16 v[116:117], v212 offset:0x2600
	v_cvt_pk_bf16_f32 v114, v115, v239
	v_add_f32_e32 v96, v96, v115
	v_add_f32_e32 v97, v97, v239
	s_add_i32 s33, s62, 0x4400
	v_mfma_f32_32x32x16_bf16 v[32:47], a[240:243], a[176:179], v[32:47]
	ds_read_b64_tr_b16 v[118:119], v212 offset:0x2e00
	ds_read_b64_tr_b16 v[104:105], v212 offset:0x3000
	v_cvt_pk_bf16_f32 v115, v240, v241
	v_add_f32_e32 v96, v96, v240
	v_add_f32_e32 v97, v97, v241
	s_mov_b32 s34, s11
	v_mfma_f32_32x32x16_bf16 v[80:95], a[212:215], a[148:151], v[80:95]
	ds_read_b64_tr_b16 v[106:107], v212 offset:0x3800
	v_add_f32_e32 v96, v96, v185
	v_add_f32_e32 v97, v97, v186
	s_add_i32 s35, s62, 0x4800
	v_mfma_f32_32x32x16_bf16 v[64:79], a[212:215], a[180:183], v[64:79]
	ds_read_b64_tr_b16 v[108:109], v212 offset:0x3200
	v_add_f32_e32 v96, v96, v187
	v_add_f32_e32 v97, v97, v188
	s_mov_b32 s36, s16
	v_mfma_f32_32x32x16_bf16 v[48:63], a[244:247], a[148:151], v[48:63]
	ds_read_b64_tr_b16 v[110:111], v212 offset:0x3a00
	v_add_f32_e32 v96, v96, v189
	v_add_f32_e32 v97, v97, v190
	s_add_i32 s37, s62, 0x4c00
	v_mfma_f32_32x32x16_bf16 v[32:47], a[244:247], a[180:183], v[32:47]
	ds_read_b64_tr_b16 v[100:101], v212 offset:0x3400
	ds_read_b64_tr_b16 v[102:103], v212 offset:0x3c00
	v_add_f32_e32 v216, v96, v191
	v_add_f32_e32 v225, v97, v192
	s_mov_b32 s38, s2
	v_mfma_f32_32x32x16_bf16 v[80:95], a[216:219], a[152:155], v[80:95]
	ds_read_b64_tr_b16 v[96:97], v212 offset:0x3600
	v_cvt_pk_bf16_f32 v140, v141, v142
	v_add_f32_e32 v226, v233, v141
	v_add_f32_e32 v142, v234, v142
	v_mfma_f32_32x32x16_bf16 v[64:79], a[216:219], a[184:187], v[64:79]
	ds_read_b64_tr_b16 v[98:99], v212 offset:0x3e00
	v_cvt_pk_bf16_f32 v141, v143, v242
	v_add_f32_e32 v143, v226, v143
	v_add_f32_e32 v226, v142, v242
	v_mfma_f32_32x32x16_bf16 v[48:63], a[248:251], a[152:155], v[48:63]
	s_add_i32 s17, s29, 0x8400
	s_mov_b32 s39, s17
	v_cvt_pk_bf16_f32 v142, v243, v244
	v_add_f32_e32 v231, v143, v243
	v_add_f32_e32 v226, v226, v244
	v_mfma_f32_32x32x16_bf16 v[32:47], a[248:251], a[184:187], v[32:47]
	s_add_i32 s40, s62, 0x80
	v_cvt_pk_bf16_f32 v143, v245, v246
	v_add_f32_e32 v231, v231, v245
	v_add_f32_e32 v226, v226, v246
	v_mfma_f32_32x32x16_bf16 v[80:95], a[220:223], a[156:159], v[80:95]
	s_add_i32 s18, s29, 0x8800
	s_mov_b32 s41, s18
	v_add_f32_e32 v231, v231, v194
	v_add_f32_e32 v226, v226, v195
	v_mfma_f32_32x32x16_bf16 v[64:79], a[220:223], a[188:191], v[64:79]
	v_add_f32_e32 v231, v231, v215
	v_add_f32_e32 v226, v226, v224
	v_mfma_f32_32x32x16_bf16 v[48:63], a[252:255], a[156:159], v[48:63]
	s_add_i32 s19, s29, 0x8c00
	s_mov_b32 s42, s19
	v_add_f32_e32 v231, v231, v227
	v_add_f32_e32 v226, v226, v228
	v_mfma_f32_32x32x16_bf16 v[32:47], a[252:255], a[188:191], v[32:47]
	s_add_i32 s43, s62, 0x880
	v_add_f32_e32 v231, v231, v229
	v_add_f32_e32 v226, v226, v230
	s_nop 0
	s_nop 4
	v_add_f32_e32 v216, v216, v225
	s_waitcnt vmcnt(0) lgkmcnt(0)
	s_barrier
	s_nop 0
	v_mov_b32_e32 v225, v216
	s_nop 1
	v_permlane32_swap_b32_e32 v216, v225
	v_add_f32_e32 v216, v216, v225
	v_add_f32_e32 v225, v193, v216
	v_add_f32_e32 v216, v231, v226
	v_mov_b32_e32 v226, v216
	s_nop 1
	v_permlane32_swap_b32_e32 v216, v226
	v_add_f32_e32 v216, v216, v226
	v_add_f32_e32 v226, v193, v216
	v_mfma_f32_32x32x16_bf16 a[0:15], v[160:163], v[152:155], 0
	s_mov_b32 m0, s27
	s_nop 0
	buffer_load_dwordx4 v222, s[12:15], s30 offen lds
	v_mfma_f32_32x32x16_bf16 a[16:31], v[160:163], v[180:183], 0
	s_mov_b32 m0, s31
	s_nop 0
	buffer_load_dwordx4 v223, s[12:15], s33 offen lds
	ds_read_b128 a[192:195], v218 offset:0
	v_mfma_f32_32x32x16_bf16 a[32:47], v[172:175], v[152:155], 0
	s_mov_b32 m0, s34
	s_nop 0
	buffer_load_dwordx4 v222, s[12:15], s35 offen lds
	ds_read_b128 a[196:199], v219 offset:0
	v_mfma_f32_32x32x16_bf16 a[48:63], v[172:175], v[180:183], 0
	s_mov_b32 m0, s36
	s_nop 0
	buffer_load_dwordx4 v223, s[12:15], s37 offen lds
	ds_read_b128 a[200:203], v220 offset:0
	v_mfma_f32_32x32x16_bf16 a[64:79], v[168:171], v[152:155], 0
	s_mov_b32 m0, s38
	s_nop 0
	buffer_load_dwordx4 v196, s[4:7], s0 offen lds
	ds_read_b128 a[204:207], v221 offset:0
	v_mfma_f32_32x32x16_bf16 a[80:95], v[168:171], v[180:183], 0
	s_mov_b32 m0, s39
	s_nop 0
	buffer_load_dwordx4 v196, s[4:7], s40 offen lds
	ds_read_b128 a[208:211], v218 offset:128
	v_mfma_f32_32x32x16_bf16 a[96:111], v[176:179], v[152:155], 0
	s_mov_b32 m0, s41
	s_nop 0
	buffer_load_dwordx4 v196, s[4:7], s1 offen lds
	ds_read_b128 a[212:215], v219 offset:128
	v_mfma_f32_32x32x16_bf16 a[112:127], v[176:179], v[180:183], 0
	s_mov_b32 m0, s42
	s_nop 0
	buffer_load_dwordx4 v196, s[4:7], s43 offen lds
	ds_read_b128 a[216:219], v220 offset:128
	v_mfma_f32_32x32x16_bf16 a[0:15], v[164:167], v[128:131], a[0:15]
	ds_read_b128 a[220:223], v221 offset:128
	v_pk_add_f32 v[200:201], v[248:249], v[200:201]
	v_pk_add_f32 v[202:203], v[250:251], v[202:203]
	v_pk_add_f32 v[204:205], v[252:253], v[204:205]
	v_pk_add_f32 v[206:207], v[254:255], v[206:207]
	v_cvt_pk_bf16_f32 v248, v248, v249
	v_cvt_pk_bf16_f32 v249, v250, v251
	v_cvt_pk_bf16_f32 v250, v252, v253
	v_cvt_pk_bf16_f32 v251, v254, v255
	v_lshrrev_b32_e32 v252, 1, v208
	buffer_store_dwordx4 v[248:251], v252, s[4:7], s56 offen sc1
	s_add_i32 s56, s56, 0x1000
	s_nop 1
	global_load_dwordx4 v[248:251], v208, s[54:55] nt
	global_load_dwordx4 v[252:255], v208, s[54:55] offset:16 nt
	s_add_u32 s54, s54, 0x2000
	s_addc_u32 s55, s55, 0
	v_max3_f32 v152, v80, v81, v48
	v_max3_f32 v153, v82, v83, v49
	v_max3_f32 v152, v152, v50, v51
	v_mfma_f32_32x32x16_bf16 a[16:31], v[164:167], v[144:147], a[16:31]
	ds_read_b128 a[224:227], v218 offset:8192
	v_max3_f32 v152, v152, v84, v85
	v_max3_f32 v153, v153, v86, v87
	v_max3_f32 v152, v152, v52, v53
	v_max3_f32 v153, v153, v54, v55
	v_mfma_f32_32x32x16_bf16 a[32:47], v[156:159], v[128:131], a[32:47]
	ds_read_b128 a[228:231], v219 offset:8192
	v_max3_f32 v152, v152, v88, v89
	v_max3_f32 v153, v153, v90, v91
	v_max3_f32 v152, v152, v56, v57
	v_max3_f32 v153, v153, v58, v59
	v_mfma_f32_32x32x16_bf16 a[48:63], v[156:159], v[144:147], a[48:63]
	ds_read_b128 a[232:235], v220 offset:8192
	v_max3_f32 v152, v152, v92, v93
	v_max3_f32 v153, v153, v94, v95
	v_max3_f32 v152, v152, v60, v61
	v_max3_f32 v153, v153, v62, v63
	v_mfma_f32_32x32x16_bf16 a[64:79], v[148:151], v[128:131], a[64:79]
	ds_read_b128 a[236:239], v221 offset:8192
	v_max3_f32 v154, v64, v65, v32
	v_max3_f32 v155, v66, v67, v33
	v_max3_f32 v154, v154, v34, v35
	v_mfma_f32_32x32x16_bf16 a[80:95], v[148:151], v[144:147], a[80:95]
	ds_read_b128 a[240:243], v218 offset:8320
	v_max3_f32 v148, v154, v68, v69
	v_max3_f32 v149, v155, v70, v71
	v_max3_f32 v148, v148, v36, v37
	v_max3_f32 v149, v149, v38, v39
	v_mfma_f32_32x32x16_bf16 a[96:111], v[136:139], v[128:131], a[96:111]
	ds_read_b128 a[244:247], v219 offset:8320
	v_max3_f32 v128, v148, v72, v73
	v_max3_f32 v129, v149, v74, v75
	v_max3_f32 v128, v128, v40, v41
	v_max3_f32 v129, v129, v42, v43
	v_mfma_f32_32x32x16_bf16 a[112:127], v[136:139], v[144:147], a[112:127]
	ds_read_b128 a[248:251], v220 offset:8320
	v_max3_f32 v128, v128, v76, v77
	v_max3_f32 v129, v129, v78, v79
	v_max3_f32 v128, v128, v44, v45
	v_max3_f32 v130, v129, v46, v47
	v_mfma_f32_32x32x16_bf16 a[0:15], v[132:135], v[112:115], a[0:15]
	ds_read_b128 a[252:255], v221 offset:8320
	v_max_f32_e32 v129, v152, v153
	v_mov_b32_e32 v131, v129
	s_nop 1
	v_permlane32_swap_b32_e32 v129, v131
	v_max_f32_e32 v129, v129, v131
	v_mfma_f32_32x32x16_bf16 a[16:31], v[132:135], v[140:143], a[16:31]
	v_max_f32_e32 v128, v128, v130
	v_mov_b32_e32 v130, v128
	s_nop 1
	v_permlane32_swap_b32_e32 v128, v130
	v_max_f32_e32 v128, v128, v130
	v_max_f32_e32 v130, v129, v129
	v_max_f32_e32 v131, v128, v128
	v_max_f32_e32 v130, v130, v131
	s_mov_b32 s0, 0x41000000
	v_mfma_f32_32x32x16_bf16 a[32:47], v[124:127], v[112:115], a[32:47]
	v_cmp_lt_f32_e32 vcc, s0, v130
	s_cmp_lg_u64 vcc, 0
	s_cselect_b64 s[0:1], -1, 0
	s_cbranch_vccnz .LBB0_41
	v_mov_b32_e32 v216, 1.0

.LBB0_17:
	v_exp_f32_e32 v48, v48
	v_exp_f32_e32 v49, v49
	v_mfma_f32_32x32x16_bf16 v[112:127], a[192:195], a[128:131], v[0:15]
	ds_read_b64_tr_b16 v[172:173], v215 offset:0
	v_cvt_pk_bf16_f32 v164, v128, v129
	v_exp_f32_e32 v50, v50
	v_exp_f32_e32 v51, v51
	v_mfma_f32_32x32x16_bf16 v[96:111], a[192:195], a[160:163], v[16:31]
	ds_read_b64_tr_b16 v[174:175], v215 offset:0x800
	v_cvt_pk_bf16_f32 v165, v130, v131
	v_mfma_f32_32x32x16_bf16 v[80:95], a[224:227], a[128:131], v[0:15]
	ds_read_b64_tr_b16 v[184:185], v215 offset:0x200
	v_exp_f32_e32 v239, v52
	v_exp_f32_e32 v240, v53
	v_cvt_pk_bf16_f32 v166, v132, v133
	v_mfma_f32_32x32x16_bf16 v[64:79], a[224:227], a[160:163], v[16:31]
	ds_read_b64_tr_b16 v[186:187], v215 offset:0xa00
	ds_read_b64_tr_b16 v[180:181], v215 offset:0x400
	v_exp_f32_e32 v241, v54
	v_exp_f32_e32 v242, v55
	v_cvt_pk_bf16_f32 v167, v134, v135
	v_exp_f32_e32 v227, v56
	v_exp_f32_e32 v228, v57
	v_mfma_f32_32x32x16_bf16 v[112:127], a[196:199], a[132:135], v[112:127]
	ds_read_b64_tr_b16 v[182:183], v215 offset:0xc00
	v_cvt_pk_bf16_f32 v128, v136, v137
	v_exp_f32_e32 v229, v58
	v_exp_f32_e32 v230, v59
	v_mfma_f32_32x32x16_bf16 v[96:111], a[196:199], a[164:167], v[96:111]
	ds_read_b64_tr_b16 v[188:189], v215 offset:0x600
	v_cvt_pk_bf16_f32 v129, v138, v139
	v_exp_f32_e32 v231, v60
	v_exp_f32_e32 v232, v61
	v_mfma_f32_32x32x16_bf16 v[80:95], a[228:231], a[132:135], v[80:95]
	ds_read_b64_tr_b16 v[190:191], v215 offset:0xe00
	v_cvt_pk_bf16_f32 v130, v140, v141
	v_mfma_f32_32x32x16_bf16 v[64:79], a[228:231], a[164:167], v[64:79]
	ds_read_b64_tr_b16 v[176:177], v215 offset:0x1000
	v_exp_f32_e32 v233, v62
	v_exp_f32_e32 v234, v63
	ds_read_b64_tr_b16 v[178:179], v215 offset:0x1800
	v_cvt_pk_bf16_f32 v131, v142, v143
	v_exp_f32_e32 v141, v32
	v_exp_f32_e32 v142, v33
	v_mfma_f32_32x32x16_bf16 v[112:127], a[200:203], a[136:139], v[112:127]
	ds_read_b64_tr_b16 v[168:169], v215 offset:0x1200
	v_cvt_pk_bf16_f32 v192, v144, v145
	v_exp_f32_e32 v143, v34
	v_mfma_f32_32x32x16_bf16 v[96:111], a[200:203], a[168:171], v[96:111]
	ds_read_b64_tr_b16 v[170:171], v215 offset:0x1a00
	v_exp_f32_e32 v243, v35
	v_cvt_pk_bf16_f32 v193, v146, v147
	v_mfma_f32_32x32x16_bf16 v[80:95], a[232:235], a[136:139], v[80:95]
	ds_read_b64_tr_b16 v[160:161], v215 offset:0x1400
	v_exp_f32_e32 v244, v36
	v_exp_f32_e32 v245, v37
	v_cvt_pk_bf16_f32 v194, v148, v149
	v_mfma_f32_32x32x16_bf16 v[64:79], a[232:235], a[168:171], v[64:79]
	ds_read_b64_tr_b16 v[162:163], v215 offset:0x1c00
	ds_read_b64_tr_b16 v[136:137], v215 offset:0x1600
	v_exp_f32_e32 v246, v38
	v_exp_f32_e32 v247, v39
	v_cvt_pk_bf16_f32 v195, v150, v151
	v_exp_f32_e32 v148, v40
	v_exp_f32_e32 v149, v41
	v_mfma_f32_32x32x16_bf16 v[112:127], a[204:207], a[140:143], v[112:127]
	ds_read_b64_tr_b16 v[138:139], v215 offset:0x1e00
	v_cvt_pk_bf16_f32 v144, v152, v153
	v_exp_f32_e32 v150, v42
	v_exp_f32_e32 v151, v43
	v_mfma_f32_32x32x16_bf16 v[96:111], a[204:207], a[172:175], v[96:111]
	ds_read_b64_tr_b16 v[132:133], v215 offset:0x2000
	v_cvt_pk_bf16_f32 v145, v154, v155
	v_exp_f32_e32 v152, v44
	v_exp_f32_e32 v153, v45
	v_mfma_f32_32x32x16_bf16 v[80:95], a[236:239], a[140:143], v[80:95]
	ds_read_b64_tr_b16 v[134:135], v215 offset:0x2800
	v_cvt_pk_bf16_f32 v146, v156, v157
	v_mfma_f32_32x32x16_bf16 v[64:79], a[236:239], a[172:175], v[64:79]
	ds_read_b64_tr_b16 v[60:61], v215 offset:0x2200
	v_exp_f32_e32 v154, v46
	v_exp_f32_e32 v155, v47
	ds_read_b64_tr_b16 v[62:63], v215 offset:0x2a00
	v_cvt_pk_bf16_f32 v147, v158, v159
	s_mov_b32 s0, s29
	v_mfma_f32_32x32x16_bf16 v[112:127], a[208:211], a[144:147], v[112:127]
	ds_read_b64_tr_b16 v[56:57], v215 offset:0x2400
	v_cvt_pk_bf16_f32 v52, v48, v49
	v_add_f32_e32 v32, v236, v48
	v_add_f32_e32 v33, v235, v49
	s_add_i32 s57, s58, s59
	s_and_b32 s57, s57, 0x7ffff
	s_mov_b32 s33, s57
	s_mov_b32 s1, s33
	v_mfma_f32_32x32x16_bf16 v[96:111], a[208:211], a[176:179], v[96:111]
	ds_read_b64_tr_b16 v[58:59], v215 offset:0x2c00
	v_cvt_pk_bf16_f32 v53, v50, v51
	v_add_f32_e32 v32, v32, v50
	v_add_f32_e32 v33, v33, v51
	s_mov_b32 s35, s20
	v_mfma_f32_32x32x16_bf16 v[80:95], a[240:243], a[144:147], v[80:95]
	ds_read_b64_tr_b16 v[48:49], v215 offset:0x2600
	v_cvt_pk_bf16_f32 v54, v239, v240
	v_add_f32_e32 v32, v32, v239
	v_add_f32_e32 v33, v33, v240
	s_add_i32 s36, s57, 0x400
	v_mfma_f32_32x32x16_bf16 v[64:79], a[240:243], a[176:179], v[64:79]
	ds_read_b64_tr_b16 v[50:51], v215 offset:0x2e00
	ds_read_b64_tr_b16 v[44:45], v215 offset:0x3000
	v_cvt_pk_bf16_f32 v55, v241, v242
	v_add_f32_e32 v32, v32, v241
	v_add_f32_e32 v33, v33, v242
	s_mov_b32 s37, s21
	v_mfma_f32_32x32x16_bf16 v[112:127], a[212:215], a[148:151], v[112:127]
	ds_read_b64_tr_b16 v[46:47], v215 offset:0x3800
	v_add_f32_e32 v32, v32, v227
	v_add_f32_e32 v33, v33, v228
	s_add_i32 s34, s57, 0x800
	s_mov_b32 s38, s34
	v_mfma_f32_32x32x16_bf16 v[96:111], a[212:215], a[180:183], v[96:111]
	ds_read_b64_tr_b16 v[40:41], v215 offset:0x3200
	v_add_f32_e32 v32, v32, v229
	v_add_f32_e32 v33, v33, v230
	s_mov_b32 s39, s22
	v_mfma_f32_32x32x16_bf16 v[80:95], a[244:247], a[148:151], v[80:95]
	ds_read_b64_tr_b16 v[42:43], v215 offset:0x3a00
	v_add_f32_e32 v32, v32, v231
	v_add_f32_e32 v33, v33, v232
	s_add_i32 s40, s57, 0xc00
	v_mfma_f32_32x32x16_bf16 v[64:79], a[244:247], a[180:183], v[64:79]
	ds_read_b64_tr_b16 v[36:37], v215 offset:0x3400
	ds_read_b64_tr_b16 v[38:39], v215 offset:0x3c00
	v_add_f32_e32 v156, v32, v233
	v_add_f32_e32 v157, v33, v234
	s_mov_b32 s41, s23
	v_mfma_f32_32x32x16_bf16 v[112:127], a[216:219], a[152:155], v[112:127]
	ds_read_b64_tr_b16 v[32:33], v215 offset:0x3600
	v_cvt_pk_bf16_f32 v140, v141, v142
	v_add_f32_e32 v158, v237, v141
	v_add_f32_e32 v142, v238, v142
	s_mov_b32 s42, s58
	v_mfma_f32_32x32x16_bf16 v[96:111], a[216:219], a[184:187], v[96:111]
	ds_read_b64_tr_b16 v[34:35], v215 offset:0x3e00
	v_cvt_pk_bf16_f32 v141, v143, v243
	v_add_f32_e32 v143, v158, v143
	v_add_f32_e32 v158, v142, v243
	v_mfma_f32_32x32x16_bf16 v[80:95], a[248:251], a[152:155], v[80:95]
	s_mov_b32 s43, s24
	v_cvt_pk_bf16_f32 v142, v244, v245
	v_add_f32_e32 v159, v143, v244
	v_add_f32_e32 v158, v158, v245
	v_mfma_f32_32x32x16_bf16 v[64:79], a[248:251], a[184:187], v[64:79]
	s_add_i32 s44, s58, 0x80
	v_cvt_pk_bf16_f32 v143, v246, v247
	v_add_f32_e32 v159, v159, v246
	v_add_f32_e32 v158, v158, v247
	v_mfma_f32_32x32x16_bf16 v[112:127], a[220:223], a[156:159], v[112:127]
	s_mov_b32 s45, s25
	v_add_f32_e32 v159, v159, v148
	v_add_f32_e32 v158, v158, v149
	v_mfma_f32_32x32x16_bf16 v[96:111], a[220:223], a[188:191], v[96:111]
	s_add_i32 s46, s58, 0x800
	v_add_f32_e32 v159, v159, v150
	v_add_f32_e32 v158, v158, v151
	v_mfma_f32_32x32x16_bf16 v[80:95], a[252:255], a[156:159], v[80:95]
	s_mov_b32 s47, s26
	v_add_f32_e32 v159, v159, v152
	v_add_f32_e32 v158, v158, v153
	v_mfma_f32_32x32x16_bf16 v[64:79], a[252:255], a[188:191], v[64:79]
	s_add_i32 s48, s58, 0x880
	v_add_f32_e32 v159, v159, v154
	v_add_f32_e32 v158, v158, v155
	s_nop 0
	s_nop 4
	v_add_f32_e32 v156, v156, v157
	s_waitcnt vmcnt(0) lgkmcnt(0)
	s_barrier
	s_nop 0
	v_mov_b32_e32 v157, v156
	s_nop 1
	v_permlane32_swap_b32_e32 v156, v157
	v_add_f32_e32 v156, v156, v157
	v_add_f32_e32 v225, v225, v156
	v_add_f32_e32 v156, v159, v158
	v_mov_b32_e32 v157, v156
	s_nop 1
	v_permlane32_swap_b32_e32 v156, v157
	v_add_f32_e32 v156, v156, v157
	v_add_f32_e32 v226, v226, v156
	v_mfma_f32_32x32x16_bf16 a[0:15], v[172:175], v[164:167], a[0:15]
	s_mov_b32 m0, s0
	s_nop 0
	buffer_load_dwordx4 v222, s[12:15], s1 offen lds
	v_mfma_f32_32x32x16_bf16 a[16:31], v[172:175], v[192:195], a[16:31]
	s_mov_b32 m0, s35
	s_nop 0
	buffer_load_dwordx4 v223, s[12:15], s36 offen lds
	ds_read_b128 a[192:195], v217 offset:0
	v_mfma_f32_32x32x16_bf16 a[32:47], v[184:187], v[164:167], a[32:47]
	s_mov_b32 m0, s37
	s_nop 0
	buffer_load_dwordx4 v222, s[12:15], s38 offen lds
	ds_read_b128 a[196:199], v199 offset:0
	v_mfma_f32_32x32x16_bf16 a[48:63], v[184:187], v[192:195], a[48:63]
	s_mov_b32 m0, s39
	s_nop 0
	buffer_load_dwordx4 v223, s[12:15], s40 offen lds
	ds_read_b128 a[200:203], v198 offset:0
	v_mfma_f32_32x32x16_bf16 a[64:79], v[180:183], v[164:167], a[64:79]
	s_mov_b32 m0, s41
	s_nop 0
	buffer_load_dwordx4 v196, s[4:7], s42 offen lds
	ds_read_b128 a[204:207], v197 offset:0
	v_mfma_f32_32x32x16_bf16 a[80:95], v[180:183], v[192:195], a[80:95]
	s_mov_b32 m0, s43
	s_nop 0
	buffer_load_dwordx4 v196, s[4:7], s44 offen lds
	ds_read_b128 a[208:211], v217 offset:128
	v_mfma_f32_32x32x16_bf16 a[96:111], v[188:191], v[164:167], a[96:111]
	s_mov_b32 m0, s45
	s_nop 0
	buffer_load_dwordx4 v196, s[4:7], s46 offen lds
	ds_read_b128 a[212:215], v199 offset:128
	v_mfma_f32_32x32x16_bf16 a[112:127], v[188:191], v[192:195], a[112:127]
	s_mov_b32 m0, s47
	s_nop 0
	buffer_load_dwordx4 v196, s[4:7], s48 offen lds
	ds_read_b128 a[216:219], v198 offset:128
	s_nop 0
	v_mfma_f32_32x32x16_bf16 a[0:15], v[176:179], v[128:131], a[0:15]
	ds_read_b128 a[220:223], v197 offset:128
	s_cmp_gt_u32 s27, 12
	s_cbranch_scc1 .Lkc_skip_a
	v_cvt_pk_bf16_f32 v248, v248, v249
	v_cvt_pk_bf16_f32 v249, v250, v251
	v_cvt_pk_bf16_f32 v250, v252, v253
	v_cvt_pk_bf16_f32 v251, v254, v255
	v_lshrrev_b32_e32 v252, 1, v208
	buffer_store_dwordx4 v[248:251], v252, s[12:15], s56 offen sc1
	s_nop 1
	global_load_dwordx4 v[248:251], v208, s[74:75] nt
	global_load_dwordx4 v[252:255], v208, s[74:75] offset:16 nt
	s_add_u32 s74, s74, 0x2000
	s_addc_u32 s75, s75, 0

.LBB0_19:
	s_waitcnt lgkmcnt(0)
	v_exp_f32_e32 v80, v80
	v_exp_f32_e32 v81, v81
	v_mfma_f32_32x32x16_bf16 v[112:127], a[192:195], a[128:131], v[0:15]
	ds_read_b64_tr_b16 v[180:181], v212 offset:0
	v_cvt_pk_bf16_f32 v168, v128, v129
	v_exp_f32_e32 v82, v82
	v_exp_f32_e32 v83, v83
	v_mfma_f32_32x32x16_bf16 v[96:111], a[192:195], a[160:163], v[16:31]
	ds_read_b64_tr_b16 v[182:183], v212 offset:0x800
	v_cvt_pk_bf16_f32 v169, v130, v131
	v_mfma_f32_32x32x16_bf16 v[48:63], a[224:227], a[128:131], v[0:15]
	ds_read_b64_tr_b16 v[184:185], v212 offset:0x200
	v_exp_f32_e32 v239, v84
	v_exp_f32_e32 v240, v85
	v_cvt_pk_bf16_f32 v170, v132, v133
	v_mfma_f32_32x32x16_bf16 v[32:47], a[224:227], a[160:163], v[16:31]
	ds_read_b64_tr_b16 v[186:187], v212 offset:0xa00
	ds_read_b64_tr_b16 v[176:177], v212 offset:0x400
	v_exp_f32_e32 v241, v86
	v_exp_f32_e32 v242, v87
	v_cvt_pk_bf16_f32 v171, v134, v135
	v_exp_f32_e32 v227, v88
	v_exp_f32_e32 v228, v89
	v_mfma_f32_32x32x16_bf16 v[112:127], a[196:199], a[132:135], v[112:127]
	ds_read_b64_tr_b16 v[178:179], v212 offset:0xc00
	v_cvt_pk_bf16_f32 v128, v136, v137
	v_exp_f32_e32 v229, v90
	v_exp_f32_e32 v230, v91
	v_mfma_f32_32x32x16_bf16 v[96:111], a[196:199], a[164:167], v[96:111]
	ds_read_b64_tr_b16 v[188:189], v212 offset:0x600
	v_cvt_pk_bf16_f32 v129, v138, v139
	v_exp_f32_e32 v231, v92
	v_exp_f32_e32 v232, v93
	v_mfma_f32_32x32x16_bf16 v[48:63], a[228:231], a[132:135], v[48:63]
	ds_read_b64_tr_b16 v[190:191], v212 offset:0xe00
	v_cvt_pk_bf16_f32 v130, v140, v141
	v_mfma_f32_32x32x16_bf16 v[32:47], a[228:231], a[164:167], v[32:47]
	ds_read_b64_tr_b16 v[172:173], v212 offset:0x1000
	v_exp_f32_e32 v233, v94
	v_exp_f32_e32 v234, v95
	ds_read_b64_tr_b16 v[174:175], v212 offset:0x1800
	v_cvt_pk_bf16_f32 v131, v142, v143
	v_exp_f32_e32 v141, v64
	v_exp_f32_e32 v142, v65
	v_mfma_f32_32x32x16_bf16 v[112:127], a[200:203], a[136:139], v[112:127]
	ds_read_b64_tr_b16 v[164:165], v212 offset:0x1200
	v_cvt_pk_bf16_f32 v192, v144, v145
	v_exp_f32_e32 v143, v66
	v_mfma_f32_32x32x16_bf16 v[96:111], a[200:203], a[168:171], v[96:111]
	ds_read_b64_tr_b16 v[166:167], v212 offset:0x1a00
	v_exp_f32_e32 v243, v67
	v_cvt_pk_bf16_f32 v193, v146, v147
	v_mfma_f32_32x32x16_bf16 v[48:63], a[232:235], a[136:139], v[48:63]
	ds_read_b64_tr_b16 v[160:161], v212 offset:0x1400
	v_exp_f32_e32 v244, v68
	v_exp_f32_e32 v245, v69
	v_cvt_pk_bf16_f32 v194, v148, v149
	v_mfma_f32_32x32x16_bf16 v[32:47], a[232:235], a[168:171], v[32:47]
	ds_read_b64_tr_b16 v[162:163], v212 offset:0x1c00
	ds_read_b64_tr_b16 v[136:137], v212 offset:0x1600
	v_exp_f32_e32 v246, v70
	v_exp_f32_e32 v247, v71
	v_cvt_pk_bf16_f32 v195, v150, v151
	v_exp_f32_e32 v148, v72
	v_exp_f32_e32 v149, v73
	v_mfma_f32_32x32x16_bf16 v[112:127], a[204:207], a[140:143], v[112:127]
	ds_read_b64_tr_b16 v[138:139], v212 offset:0x1e00
	v_cvt_pk_bf16_f32 v144, v152, v153
	v_exp_f32_e32 v150, v74
	v_exp_f32_e32 v151, v75
	v_mfma_f32_32x32x16_bf16 v[96:111], a[204:207], a[172:175], v[96:111]
	ds_read_b64_tr_b16 v[132:133], v212 offset:0x2000
	v_cvt_pk_bf16_f32 v145, v154, v155
	v_exp_f32_e32 v152, v76
	v_exp_f32_e32 v153, v77
	v_mfma_f32_32x32x16_bf16 v[48:63], a[236:239], a[140:143], v[48:63]
	ds_read_b64_tr_b16 v[134:135], v212 offset:0x2800
	v_cvt_pk_bf16_f32 v146, v156, v157
	v_mfma_f32_32x32x16_bf16 v[32:47], a[236:239], a[172:175], v[32:47]
	ds_read_b64_tr_b16 v[92:93], v212 offset:0x2200
	v_exp_f32_e32 v154, v78
	v_exp_f32_e32 v155, v79
	ds_read_b64_tr_b16 v[94:95], v212 offset:0x2a00
	v_cvt_pk_bf16_f32 v147, v158, v159
	s_mov_b32 s0, s3
	v_mfma_f32_32x32x16_bf16 v[112:127], a[208:211], a[144:147], v[112:127]
	ds_read_b64_tr_b16 v[88:89], v212 offset:0x2400
	v_cvt_pk_bf16_f32 v84, v80, v81
	v_add_f32_e32 v64, v236, v80
	v_add_f32_e32 v65, v235, v81
	s_add_i32 s58, s57, s60
	s_and_b32 s58, s58, 0x7ffff
	s_mov_b32 s1, s58
	v_mfma_f32_32x32x16_bf16 v[96:111], a[208:211], a[176:179], v[96:111]
	ds_read_b64_tr_b16 v[90:91], v212 offset:0x2c00
	v_cvt_pk_bf16_f32 v85, v82, v83
	v_add_f32_e32 v64, v64, v82
	v_add_f32_e32 v65, v65, v83
	s_mov_b32 s35, s10
	v_mfma_f32_32x32x16_bf16 v[48:63], a[240:243], a[144:147], v[48:63]
	ds_read_b64_tr_b16 v[80:81], v212 offset:0x2600
	v_cvt_pk_bf16_f32 v86, v239, v240
	v_add_f32_e32 v64, v64, v239
	v_add_f32_e32 v65, v65, v240
	s_add_i32 s36, s58, 0x400
	v_mfma_f32_32x32x16_bf16 v[32:47], a[240:243], a[176:179], v[32:47]
	ds_read_b64_tr_b16 v[82:83], v212 offset:0x2e00
	ds_read_b64_tr_b16 v[76:77], v212 offset:0x3000
	v_cvt_pk_bf16_f32 v87, v241, v242
	v_add_f32_e32 v64, v64, v241
	v_add_f32_e32 v65, v65, v242
	s_mov_b32 s37, s11
	v_mfma_f32_32x32x16_bf16 v[112:127], a[212:215], a[148:151], v[112:127]
	ds_read_b64_tr_b16 v[78:79], v212 offset:0x3800
	v_add_f32_e32 v64, v64, v227
	v_add_f32_e32 v65, v65, v228
	s_add_i32 s38, s58, 0x800
	v_mfma_f32_32x32x16_bf16 v[96:111], a[212:215], a[180:183], v[96:111]
	ds_read_b64_tr_b16 v[72:73], v212 offset:0x3200
	v_add_f32_e32 v64, v64, v229
	v_add_f32_e32 v65, v65, v230
	s_mov_b32 s39, s16
	v_mfma_f32_32x32x16_bf16 v[48:63], a[244:247], a[148:151], v[48:63]
	ds_read_b64_tr_b16 v[74:75], v212 offset:0x3a00
	v_add_f32_e32 v64, v64, v231
	v_add_f32_e32 v65, v65, v232
	s_add_i32 s40, s58, 0xc00
	v_mfma_f32_32x32x16_bf16 v[32:47], a[244:247], a[180:183], v[32:47]
	ds_read_b64_tr_b16 v[68:69], v212 offset:0x3400
	ds_read_b64_tr_b16 v[70:71], v212 offset:0x3c00
	v_add_f32_e32 v156, v64, v233
	v_add_f32_e32 v157, v65, v234
	s_mov_b32 s41, s2
	v_mfma_f32_32x32x16_bf16 v[112:127], a[216:219], a[152:155], v[112:127]
	ds_read_b64_tr_b16 v[64:65], v212 offset:0x3600
	v_cvt_pk_bf16_f32 v140, v141, v142
	v_add_f32_e32 v158, v237, v141
	v_add_f32_e32 v142, v238, v142
	v_mfma_f32_32x32x16_bf16 v[96:111], a[216:219], a[184:187], v[96:111]
	ds_read_b64_tr_b16 v[66:67], v212 offset:0x3e00
	v_cvt_pk_bf16_f32 v141, v143, v243
	v_add_f32_e32 v143, v158, v143
	v_add_f32_e32 v158, v142, v243
	v_mfma_f32_32x32x16_bf16 v[48:63], a[248:251], a[152:155], v[48:63]
	s_mov_b32 s42, s17
	v_cvt_pk_bf16_f32 v142, v244, v245
	v_add_f32_e32 v159, v143, v244
	v_add_f32_e32 v158, v158, v245
	v_mfma_f32_32x32x16_bf16 v[32:47], a[248:251], a[184:187], v[32:47]
	s_add_i32 s43, s57, 0x80
	v_cvt_pk_bf16_f32 v143, v246, v247
	v_add_f32_e32 v159, v159, v246
	v_add_f32_e32 v158, v158, v247
	v_mfma_f32_32x32x16_bf16 v[112:127], a[220:223], a[156:159], v[112:127]
	s_mov_b32 s44, s18
	v_add_f32_e32 v159, v159, v148
	v_add_f32_e32 v158, v158, v149
	v_mfma_f32_32x32x16_bf16 v[96:111], a[220:223], a[188:191], v[96:111]
	v_add_f32_e32 v159, v159, v150
	v_add_f32_e32 v158, v158, v151
	v_mfma_f32_32x32x16_bf16 v[48:63], a[252:255], a[156:159], v[48:63]
	s_mov_b32 s45, s19
	v_add_f32_e32 v159, v159, v152
	v_add_f32_e32 v158, v158, v153
	v_mfma_f32_32x32x16_bf16 v[32:47], a[252:255], a[188:191], v[32:47]
	s_add_i32 s46, s57, 0x880
	v_add_f32_e32 v159, v159, v154
	v_add_f32_e32 v158, v158, v155
	s_nop 0
	s_nop 4
	v_add_f32_e32 v156, v156, v157
	s_waitcnt vmcnt(0) lgkmcnt(0)
	s_barrier
	s_nop 0
	v_mov_b32_e32 v157, v156
	s_nop 1
	v_permlane32_swap_b32_e32 v156, v157
	v_add_f32_e32 v156, v156, v157
	v_add_f32_e32 v225, v225, v156
	v_add_f32_e32 v156, v159, v158
	v_mov_b32_e32 v157, v156
	s_nop 1
	v_permlane32_swap_b32_e32 v156, v157
	v_add_f32_e32 v156, v156, v157
	v_add_f32_e32 v226, v226, v156
	v_mfma_f32_32x32x16_bf16 a[0:15], v[180:183], v[168:171], a[0:15]
	s_mov_b32 m0, s0
	s_nop 0
	buffer_load_dwordx4 v222, s[12:15], s1 offen lds
	v_mfma_f32_32x32x16_bf16 a[16:31], v[180:183], v[192:195], a[16:31]
	s_mov_b32 m0, s35
	s_nop 0
	buffer_load_dwordx4 v223, s[12:15], s36 offen lds
	ds_read_b128 a[192:195], v218 offset:0
	v_mfma_f32_32x32x16_bf16 a[32:47], v[184:187], v[168:171], a[32:47]
	s_mov_b32 m0, s37
	s_nop 0
	buffer_load_dwordx4 v222, s[12:15], s38 offen lds
	ds_read_b128 a[196:199], v219 offset:0
	v_mfma_f32_32x32x16_bf16 a[48:63], v[184:187], v[192:195], a[48:63]
	s_mov_b32 m0, s39
	s_nop 0
	buffer_load_dwordx4 v223, s[12:15], s40 offen lds
	ds_read_b128 a[200:203], v220 offset:0
	v_mfma_f32_32x32x16_bf16 a[64:79], v[176:179], v[168:171], a[64:79]
	s_mov_b32 m0, s41
	s_nop 0
	buffer_load_dwordx4 v196, s[4:7], s33 offen lds
	ds_read_b128 a[204:207], v221 offset:0
	v_mfma_f32_32x32x16_bf16 a[80:95], v[176:179], v[192:195], a[80:95]
	s_mov_b32 m0, s42
	s_nop 0
	buffer_load_dwordx4 v196, s[4:7], s43 offen lds
	ds_read_b128 a[208:211], v218 offset:128
	v_mfma_f32_32x32x16_bf16 a[96:111], v[188:191], v[168:171], a[96:111]
	s_mov_b32 m0, s44
	s_nop 0
	buffer_load_dwordx4 v196, s[4:7], s34 offen lds
	ds_read_b128 a[212:215], v219 offset:128
	v_mfma_f32_32x32x16_bf16 a[112:127], v[188:191], v[192:195], a[112:127]
	s_mov_b32 m0, s45
	s_nop 0
	buffer_load_dwordx4 v196, s[4:7], s46 offen lds
	ds_read_b128 a[216:219], v220 offset:128
	s_nop 0
	v_mfma_f32_32x32x16_bf16 a[0:15], v[172:175], v[128:131], a[0:15]
	ds_read_b128 a[220:223], v221 offset:128
	s_cmp_gt_u32 s27, 12
	s_cbranch_scc1 .Lkc_skip_b
	v_pk_add_f32 v[200:201], v[248:249], v[200:201]
	v_pk_add_f32 v[202:203], v[250:251], v[202:203]
	v_pk_add_f32 v[204:205], v[252:253], v[204:205]
	v_pk_add_f32 v[206:207], v[254:255], v[206:207]
	v_cvt_pk_bf16_f32 v248, v248, v249
	v_cvt_pk_bf16_f32 v249, v250, v251
	v_cvt_pk_bf16_f32 v250, v252, v253
	v_cvt_pk_bf16_f32 v251, v254, v255
	v_lshrrev_b32_e32 v252, 1, v208
	buffer_store_dwordx4 v[248:251], v252, s[4:7], s56 offen sc1
	s_add_i32 s56, s56, 0x1000
	s_cmp_gt_u32 s27, 10
	s_cbranch_scc1 .Lkc_skip_b
	s_nop 1
	global_load_dwordx4 v[248:251], v208, s[54:55] nt
	global_load_dwordx4 v[252:255], v208, s[54:55] offset:16 nt
	s_add_u32 s54, s54, 0x2000
	s_addc_u32 s55, s55, 0

.Ltail_events:
	s_cmp_eq_u32 s27, 8
	s_cbranch_scc1 .Ltail_pub2
	s_cmp_eq_u32 s27, 10
	s_cbranch_scc1 .Ltail_smp2
	s_cmp_eq_u32 s27, 14
	s_cbranch_scc1 .Ltail_cs
	s_cmp_eq_u32 s27, 16
	s_cbranch_scc1 .Ltail_pub3
	s_cmp_eq_u32 s27, 18
	s_cbranch_scc1 .Ltail_smp3
	s_mov_b32 s59, s69
	s_mov_b32 s53, 0x10000
	s_cmp_eq_u32 s27, 12
	s_cbranch_scc0 .Ltail_chk3

.Ltail_cs:
	v_lshrrev_b32_e32 v248, 9, v208
	v_mul_u32_u24_e32 v248, 0x210, v248
	v_and_b32_e32 v249, 0x1e0, v208
	v_add_u32_e32 v248, v248, v249
	v_add_u32_e32 v248, 0x20000, v248
	ds_write_b128 v248, v[200:203]
	ds_write_b128 v248, v[204:207] offset:16
	s_branch .Ltail_resume
.Ltail_pub3:
	s_cmp_gt_u32 s50, 1
	s_cbranch_scc1 .Ltail_resume
	v_mbcnt_lo_u32_b32 v210, -1, 0
	v_mbcnt_hi_u32_b32 v210, -1, v210
	s_lshl_b32 s53, s50, 8
	v_lshlrev_b32_e32 v210, 2, v210
	v_add_u32_e32 v210, s53, v210
	v_add_u32_e32 v249, 0x20000, v210
	ds_read_b32 v200, v249 offset:0
	ds_read_b32 v201, v249 offset:528
	ds_read_b32 v202, v249 offset:1056
	ds_read_b32 v203, v249 offset:1584
	ds_read_b32 v204, v249 offset:2112
	ds_read_b32 v205, v249 offset:2640
	ds_read_b32 v206, v249 offset:3168
	ds_read_b32 v207, v249 offset:3696
	ds_read_b32 v250, v249 offset:4224
	ds_read_b32 v251, v249 offset:4752
	ds_read_b32 v252, v249 offset:5280
	ds_read_b32 v253, v249 offset:5808
	ds_read_b32 v254, v249 offset:6336
	ds_read_b32 v255, v249 offset:6864
	ds_read_b32 v248, v249 offset:7392
	s_waitcnt lgkmcnt(0)
	v_add_f32_e32 v200, 0, v200
	v_add_f32_e32 v200, v200, v201
	v_add_f32_e32 v200, v200, v202
	v_add_f32_e32 v200, v200, v203
	v_add_f32_e32 v200, v200, v204
	v_add_f32_e32 v200, v200, v205
	v_add_f32_e32 v200, v200, v206
	v_add_f32_e32 v200, v200, v207
	v_add_f32_e32 v200, v200, v250
	v_add_f32_e32 v200, v200, v251
	v_add_f32_e32 v200, v200, v252
	v_add_f32_e32 v200, v200, v253
	v_add_f32_e32 v200, v200, v254
	v_add_f32_e32 v200, v200, v255
	v_add_f32_e32 v200, v200, v248
	ds_read_b32 v201, v249 offset:7920
	s_waitcnt lgkmcnt(0)
	v_add_f32_e32 v200, v200, v201
	global_store_dword v210, v200, s[76:77] sc1
	s_cmp_eq_u32 s50, 0
	s_cbranch_scc0 .Ltail_resume
	v_mov_b32_e32 v201, s70
	s_mov_b64 exec, 1
	global_store_dword v209, v201, s[72:73] offset:2048 sc1
	s_mov_b64 exec, -1
	s_branch .Ltail_resume

	.amdhsa_kernel attn_fwd_pwg4x64
		.amdhsa_group_segment_fixed_size 0
		.amdhsa_private_segment_fixed_size 0
		.amdhsa_kernarg_size 72
		.amdhsa_user_sgpr_count 2
		.amdhsa_user_sgpr_dispatch_ptr 0
		.amdhsa_user_sgpr_queue_ptr 0
		.amdhsa_user_sgpr_kernarg_segment_ptr 1
		.amdhsa_user_sgpr_dispatch_id 0
		.amdhsa_user_sgpr_kernarg_preload_length 0
		.amdhsa_user_sgpr_kernarg_preload_offset 0
		.amdhsa_user_sgpr_private_segment_size 0
		.amdhsa_uses_dynamic_stack 0
		.amdhsa_enable_private_segment 0
		.amdhsa_system_sgpr_workgroup_id_x 1
		.amdhsa_system_sgpr_workgroup_id_y 0
		.amdhsa_system_sgpr_workgroup_id_z 0
		.amdhsa_system_sgpr_workgroup_info 0
		.amdhsa_system_vgpr_workitem_id 0
		.amdhsa_next_free_vgpr 512
		.amdhsa_next_free_sgpr 78
		.amdhsa_accum_offset 256
		.amdhsa_reserve_vcc 1
		.amdhsa_float_round_mode_32 0
		.amdhsa_float_round_mode_16_64 0
		.amdhsa_float_denorm_mode_32 3
		.amdhsa_float_denorm_mode_16_64 3
		.amdhsa_dx10_clamp 1
		.amdhsa_ieee_mode 1
		.amdhsa_fp16_overflow 0
		.amdhsa_tg_split 0
		.amdhsa_exception_fp_ieee_invalid_op 0
		.amdhsa_exception_fp_denorm_src 0
		.amdhsa_exception_fp_ieee_div_zero 0
		.amdhsa_exception_fp_ieee_overflow 0
		.amdhsa_exception_fp_ieee_underflow 0
		.amdhsa_exception_fp_ieee_inexact 0
		.amdhsa_exception_int_div_zero 0
	.end_amdhsa_kernel

.LBB1_2:
	s_lshl_b64 s[8:9], s[2:3], 8
	s_lshr_b64 s[6:7], s[8:9], 11
	s_and_b32 s2, s6, 0x1ffffff0
	v_or_b32_e32 v66, s8, v0
	s_lshl_b64 s[10:11], s[2:3], 19
	v_and_b32_e32 v1, 0x7fff, v66
	s_waitcnt lgkmcnt(0)
	s_add_u32 s4, s4, s10
	s_addc_u32 s5, s5, s11
	v_lshlrev_b32_e32 v68, 4, v1
	v_lshl_add_u64 v[14:15], s[4:5], 0, v[68:69]
	s_mov_b32 s8, 0x80000
	v_add_co_u32_e32 v2, vcc, s8, v14
	s_mov_b32 s8, 0x100000
	s_nop 0
	v_addc_co_u32_e32 v3, vcc, 0, v15, vcc
	v_add_co_u32_e32 v4, vcc, s8, v14
	s_mov_b32 s8, 0x180000
	s_nop 0
	v_addc_co_u32_e32 v5, vcc, 0, v15, vcc
	global_load_dwordx4 v[42:45], v[2:3], off
	global_load_dwordx4 v[34:37], v[4:5], off
	v_add_co_u32_e32 v2, vcc, s8, v14
	s_mov_b32 s8, 0x200000
	s_nop 0
	v_addc_co_u32_e32 v3, vcc, 0, v15, vcc
	v_add_co_u32_e32 v4, vcc, s8, v14
	s_mov_b32 s8, 0x280000
	s_nop 0
	v_addc_co_u32_e32 v5, vcc, 0, v15, vcc
	global_load_dwordx4 v[58:61], v[2:3], off
	global_load_dwordx4 v[46:49], v[4:5], off
	v_add_co_u32_e32 v2, vcc, s8, v14
	s_mov_b32 s8, 0x300000
	s_nop 0
	v_addc_co_u32_e32 v3, vcc, 0, v15, vcc
	v_add_co_u32_e32 v4, vcc, s8, v14
	s_mov_b32 s8, 0x380000
	s_nop 0
	v_addc_co_u32_e32 v5, vcc, 0, v15, vcc
	v_add_co_u32_e32 v6, vcc, s8, v14
	s_mov_b32 s8, 0x400000
	s_nop 0
	v_addc_co_u32_e32 v7, vcc, 0, v15, vcc
	v_add_co_u32_e32 v8, vcc, s8, v14
	s_mov_b32 s8, 0x480000
	s_nop 0
	v_addc_co_u32_e32 v9, vcc, 0, v15, vcc
	v_add_co_u32_e32 v16, vcc, s8, v14
	s_mov_b32 s8, 0x500000
	s_nop 0
	v_addc_co_u32_e32 v17, vcc, 0, v15, vcc
	v_add_co_u32_e32 v18, vcc, s8, v14
	s_mov_b32 s8, 0x580000
	s_nop 0
	v_addc_co_u32_e32 v19, vcc, 0, v15, vcc
	v_add_co_u32_e32 v70, vcc, s8, v14
	s_mov_b32 s8, 0x600000
	s_nop 0
	v_addc_co_u32_e32 v71, vcc, 0, v15, vcc
	v_add_co_u32_e32 v72, vcc, s8, v14
	s_mov_b32 s8, 0x680000
	s_nop 0
	v_addc_co_u32_e32 v73, vcc, 0, v15, vcc
	v_add_co_u32_e32 v74, vcc, s8, v14
	global_load_dwordx4 v[54:57], v[2:3], off
	global_load_dwordx4 v[38:41], v[4:5], off
	v_addc_co_u32_e32 v75, vcc, 0, v15, vcc
	v_add_co_u32_e32 v76, vcc, 0x700000, v14
	global_load_dwordx4 v[50:53], v[6:7], off
	global_load_dwordx4 v[2:5], v[8:9], off
	v_addc_co_u32_e32 v77, vcc, 0, v15, vcc
	v_add_co_u32_e32 v78, vcc, 0x780000, v14
	global_load_dwordx4 v[10:13], v[16:17], off
	global_load_dwordx4 v[6:9], v[18:19], off
	v_addc_co_u32_e32 v79, vcc, 0, v15, vcc
	global_load_dwordx4 v[30:33], v[70:71], off
	global_load_dwordx4 v[22:25], v[72:73], off
	global_load_dwordx4 v[26:29], v[74:75], off
	global_load_dwordx4 v[18:21], v[76:77], off
	global_load_dwordx4 v[62:65], v68, s[4:5]
	global_load_dwordx4 v[14:17], v[78:79], off
	s_load_dwordx2 s[4:5], s[0:1], 0x18
	v_mov_b32_e32 v67, s9
	s_load_dwordx2 s[12:13], s[0:1], 0x8
	v_and_b32_e32 v70, 31, v0
	v_lshlrev_b32_e32 v70, 4, v70
	v_lshrrev_b32_e32 v71, 5, v0
	v_lshl_or_b32 v72, v71, 13, v70
	v_lshl_or_b32 v73, v71, 9, v70
	s_waitcnt lgkmcnt(0)
	s_lshl_b32 s14, s2, 12
	s_sub_u32 s12, s12, 0x20000
	s_subb_u32 s13, s13, 0
	s_add_u32 s12, s12, s14
	s_addc_u32 s13, s13, 0
	s_add_u32 s14, s12, 0x1000
	s_addc_u32 s15, s13, 0
	global_load_dwordx4 v[88:91], v72, s[12:13] offset:0
	global_load_dwordx4 v[92:95], v72, s[12:13] offset:512
	global_load_dwordx4 v[96:99], v72, s[12:13] offset:1024
	global_load_dwordx4 v[100:103], v72, s[12:13] offset:1536
	global_load_dwordx4 v[104:107], v72, s[12:13] offset:2048
	global_load_dwordx4 v[108:111], v72, s[12:13] offset:2560
	global_load_dwordx4 v[112:115], v72, s[12:13] offset:3072
	global_load_dwordx4 v[116:119], v72, s[12:13] offset:3584
	global_load_dwordx4 v[120:123], v72, s[14:15] offset:0
	global_load_dwordx4 v[124:127], v72, s[14:15] offset:512
	global_load_dwordx4 v[128:131], v72, s[14:15] offset:1024
	global_load_dwordx4 v[132:135], v72, s[14:15] offset:1536
	global_load_dwordx4 v[136:139], v72, s[14:15] offset:2048
	global_load_dwordx4 v[140:143], v72, s[14:15] offset:2560
	global_load_dwordx4 v[144:147], v72, s[14:15] offset:3072
	global_load_dwordx4 v[148:151], v72, s[14:15] offset:3584
	s_waitcnt vmcnt(15)
	s_waitcnt vmcnt(14)
	v_pk_add_f32 v[88:89], v[88:89], v[92:93]
	v_pk_add_f32 v[90:91], v[90:91], v[94:95]
	s_waitcnt vmcnt(13)
	v_pk_add_f32 v[88:89], v[88:89], v[96:97]
	v_pk_add_f32 v[90:91], v[90:91], v[98:99]
	s_waitcnt vmcnt(12)
	v_pk_add_f32 v[88:89], v[88:89], v[100:101]
	v_pk_add_f32 v[90:91], v[90:91], v[102:103]
	s_waitcnt vmcnt(11)
	v_pk_add_f32 v[88:89], v[88:89], v[104:105]
	v_pk_add_f32 v[90:91], v[90:91], v[106:107]
	s_waitcnt vmcnt(10)
	v_pk_add_f32 v[88:89], v[88:89], v[108:109]
	v_pk_add_f32 v[90:91], v[90:91], v[110:111]
	s_waitcnt vmcnt(9)
	v_pk_add_f32 v[88:89], v[88:89], v[112:113]
	v_pk_add_f32 v[90:91], v[90:91], v[114:115]
	s_waitcnt vmcnt(8)
	v_pk_add_f32 v[88:89], v[88:89], v[116:117]
	v_pk_add_f32 v[90:91], v[90:91], v[118:119]
	s_waitcnt vmcnt(7)
	v_pk_add_f32 v[88:89], v[88:89], v[120:121]
	v_pk_add_f32 v[90:91], v[90:91], v[122:123]
	s_waitcnt vmcnt(6)
	v_pk_add_f32 v[88:89], v[88:89], v[124:125]
	v_pk_add_f32 v[90:91], v[90:91], v[126:127]
	s_waitcnt vmcnt(5)
	v_pk_add_f32 v[88:89], v[88:89], v[128:129]
	v_pk_add_f32 v[90:91], v[90:91], v[130:131]
	s_waitcnt vmcnt(4)
	v_pk_add_f32 v[88:89], v[88:89], v[132:133]
	v_pk_add_f32 v[90:91], v[90:91], v[134:135]
	s_waitcnt vmcnt(3)
	v_pk_add_f32 v[88:89], v[88:89], v[136:137]
	v_pk_add_f32 v[90:91], v[90:91], v[138:139]
	s_waitcnt vmcnt(2)
	v_pk_add_f32 v[88:89], v[88:89], v[140:141]
	v_pk_add_f32 v[90:91], v[90:91], v[142:143]
	s_waitcnt vmcnt(1)
	v_pk_add_f32 v[88:89], v[88:89], v[144:145]
	v_pk_add_f32 v[90:91], v[90:91], v[146:147]
	s_waitcnt vmcnt(0)
	v_pk_add_f32 v[88:89], v[88:89], v[148:149]
	v_pk_add_f32 v[90:91], v[90:91], v[150:151]
	ds_write_b128 v73, v[88:91] offset:512
	s_waitcnt lgkmcnt(0)
	s_barrier
	s_movk_i32 s8, 0x80
	v_cmp_gt_u32_e32 vcc, s8, v0
	s_and_saveexec_b64 s[8:9], vcc
	s_cbranch_execz .LBB1_4
	v_lshlrev_b32_e32 v68, 2, v0
	ds_read_b32 v74, v68 offset:512
	ds_read_b32 v75, v68 offset:1024
	ds_read_b32 v76, v68 offset:1536
	ds_read_b32 v77, v68 offset:2048
	ds_read_b32 v78, v68 offset:2560
	ds_read_b32 v79, v68 offset:3072
	ds_read_b32 v80, v68 offset:3584
	ds_read_b32 v81, v68 offset:4096
	s_waitcnt lgkmcnt(0)
	v_add_f32_e32 v1, 0, v74
	v_add_f32_e32 v1, v1, v75
	v_add_f32_e32 v1, v1, v76
	v_add_f32_e32 v1, v1, v77
	v_add_f32_e32 v1, v1, v78
	v_add_f32_e32 v1, v1, v79
	v_add_f32_e32 v1, v1, v80
	v_add_f32_e32 v1, v1, v81
	v_mul_f32_e32 v1, 0x3bf00000, v1
	ds_write_b32 v68, v1

	.amdhsa_kernel _Z14headsum_kernelPKtPKfPjPf
		.amdhsa_group_segment_fixed_size 4608
		.amdhsa_private_segment_fixed_size 0
		.amdhsa_kernarg_size 32
		.amdhsa_user_sgpr_count 2
		.amdhsa_user_sgpr_dispatch_ptr 0
		.amdhsa_user_sgpr_queue_ptr 0
		.amdhsa_user_sgpr_kernarg_segment_ptr 1
		.amdhsa_user_sgpr_dispatch_id 0
		.amdhsa_user_sgpr_kernarg_preload_length 0
		.amdhsa_user_sgpr_kernarg_preload_offset 0
		.amdhsa_user_sgpr_private_segment_size 0
		.amdhsa_uses_dynamic_stack 0
		.amdhsa_enable_private_segment 0
		.amdhsa_system_sgpr_workgroup_id_x 1
		.amdhsa_system_sgpr_workgroup_id_y 0
		.amdhsa_system_sgpr_workgroup_id_z 0
		.amdhsa_system_sgpr_workgroup_info 0
		.amdhsa_system_vgpr_workitem_id 0
		.amdhsa_next_free_vgpr 152
		.amdhsa_next_free_sgpr 16
		.amdhsa_accum_offset 152
		.amdhsa_reserve_vcc 1
		.amdhsa_float_round_mode_32 0
		.amdhsa_float_round_mode_16_64 0
		.amdhsa_float_denorm_mode_32 3
		.amdhsa_float_denorm_mode_16_64 3
		.amdhsa_dx10_clamp 1
		.amdhsa_ieee_mode 1
		.amdhsa_fp16_overflow 0
		.amdhsa_tg_split 0
		.amdhsa_exception_fp_ieee_invalid_op 0
		.amdhsa_exception_fp_denorm_src 0
		.amdhsa_exception_fp_ieee_div_zero 0
		.amdhsa_exception_fp_ieee_overflow 0
		.amdhsa_exception_fp_ieee_underflow 0
		.amdhsa_exception_fp_ieee_inexact 0
		.amdhsa_exception_int_div_zero 0
	.end_amdhsa_kernel

amdhsa.kernels:
  - .agpr_count:     256
    .args:
      - .actual_access:  read_only
        .address_space:  global
        .offset:         0
        .size:           8
        .value_kind:     global_buffer
      - .address_space:  global
        .offset:         8
        .size:           8
        .value_kind:     global_buffer
      - .address_space:  global
        .offset:         16
        .size:           8
        .value_kind:     global_buffer
      - .actual_access:  write_only
        .address_space:  global
        .offset:         24
        .size:           8
        .value_kind:     global_buffer
      - .actual_access:  read_only
        .address_space:  global
        .offset:         32
        .size:           8
        .value_kind:     global_buffer
      - .actual_access:  read_only
        .address_space:  global
        .offset:         40
        .size:           8
        .value_kind:     global_buffer
      - .address_space:  global
        .offset:         48
        .size:           8
        .value_kind:     global_buffer
      - .address_space:  global
        .offset:         56
        .size:           8
        .value_kind:     global_buffer
      - .actual_access:  write_only
        .address_space:  global
        .offset:         64
        .size:           8
        .value_kind:     global_buffer
    .group_segment_fixed_size: 0
    .kernarg_segment_align: 8
    .kernarg_segment_size: 72
    .language:       OpenCL C
    .language_version:
      - 2
      - 0
    .max_flat_workgroup_size: 256
    .name:           attn_fwd_pwg4x64
    .private_segment_fixed_size: 0
    .sgpr_count:     84
    .sgpr_spill_count: 0
    .symbol:         attn_fwd_pwg4x64.kd
    .uniform_work_group_size: 1
    .uses_dynamic_stack: false
    .vgpr_count:     512
    .vgpr_spill_count: 0
    .wavefront_size: 64
  - .agpr_count:     0
    .args:
      - .actual_access:  read_only
        .address_space:  global
        .offset:         0
        .size:           8
        .value_kind:     global_buffer
      - .actual_access:  read_only
        .address_space:  global
        .offset:         8
        .size:           8
        .value_kind:     global_buffer
      - .actual_access:  write_only
        .address_space:  global
        .offset:         16
        .size:           8
        .value_kind:     global_buffer
      - .actual_access:  write_only
        .address_space:  global
        .offset:         24
        .size:           8
        .value_kind:     global_buffer
    .group_segment_fixed_size: 4608
    .kernarg_segment_align: 8
    .kernarg_segment_size: 32
    .language:       OpenCL C
    .language_version:
      - 2
      - 0
    .max_flat_workgroup_size: 256
    .name:           _Z14headsum_kernelPKtPKfPjPf
    .private_segment_fixed_size: 0
    .sgpr_count:     22
    .sgpr_spill_count: 0
    .symbol:         _Z14headsum_kernelPKtPKfPjPf.kd
    .uniform_work_group_size: 1
    .uses_dynamic_stack: false
    .vgpr_count:     152
    .vgpr_spill_count: 0
    .wavefront_size: 64
